# MoE M2 publish: H rows stored write-through (sc0 sc1), per-unit L2 write-back dropped (sc1 payload -> vmcnt(0) -> flag); table-build expert search reads prefetched
# speedup vs baseline: 1.0212x; 1.0212x over previous
.LBB0_1077:
	s_or_b64 exec, exec, s[4:5]
	s_add_u32 s14, s8, 0x5e140000
	s_addc_u32 s15, s9, 0
	s_add_u32 s12, s8, 0x5e240000
	s_addc_u32 s13, s9, 0
	s_lshl_b32 s4, s6, 5
	s_and_b32 s4, s4, 0xe0
	s_ashr_i32 s5, s6, 3
	s_add_i32 s4, s4, s5
	s_cmpk_eq_i32 s22, 0x100
	s_cselect_b32 s23, s4, s6
	s_cmp_gt_i32 s23, -1
	s_cselect_b64 s[6:7], -1, 0
	s_cmp_lt_i32 s23, 0
	s_mov_b32 s18, 0
	s_waitcnt lgkmcnt(0)
	s_barrier
	s_cbranch_scc1 .LBB0_1087
	v_readlane_b32 s4, v255, 3
	s_nop 1
	v_mov_b32_e32 v0, s4
	ds_read_b32 v0, v0
	s_waitcnt lgkmcnt(0)
	v_cmp_ge_i32_e32 vcc, s23, v0
	s_cbranch_vccnz .LBB0_1087
	s_movk_i32 s4, 0x100
	v_cmp_gt_i32_e32 vcc, s4, v206
	s_and_saveexec_b64 s[4:5], vcc
	s_cbranch_execz .LBB0_1086
	v_readlane_b32 s16, v255, 4
	v_mov_b32_e32 v208, -1
	s_nop 0
	v_readlane_b32 s100, v255, 4
	s_nop 1
	v_mov_b32_e32 v214, s100
	ds_read2_b32 v[128:129], v214 offset1:1
	v_readlane_b32 s100, v254, 45
	s_nop 1
	v_mov_b32_e32 v214, s100
	ds_read2_b32 v[130:131], v214 offset1:1
	v_readlane_b32 s100, v254, 47
	s_nop 1
	v_mov_b32_e32 v214, s100
	ds_read2_b32 v[132:133], v214 offset1:1
	v_readlane_b32 s100, v254, 48
	s_nop 1
	v_mov_b32_e32 v214, s100
	ds_read2_b32 v[134:135], v214 offset1:1
	v_readlane_b32 s100, v254, 50
	s_nop 1
	v_mov_b32_e32 v214, s100
	ds_read2_b32 v[136:137], v214 offset1:1
	v_readlane_b32 s100, v254, 51
	s_nop 1
	v_mov_b32_e32 v214, s100
	ds_read2_b32 v[138:139], v214 offset1:1
	v_readlane_b32 s100, v254, 53
	s_nop 1
	v_mov_b32_e32 v214, s100
	ds_read2_b32 v[140:141], v214 offset1:1
	v_readlane_b32 s100, v254, 54
	s_nop 1
	v_mov_b32_e32 v214, s100
	ds_read2_b32 v[142:143], v214 offset1:1
	s_waitcnt lgkmcnt(0)
	v_readlane_b32 s100, v254, 56
	s_nop 1
	v_mov_b32_e32 v214, s100
	ds_read2_b32 v[144:145], v214 offset1:1
	v_readlane_b32 s100, v254, 57
	s_nop 1
	v_mov_b32_e32 v214, s100
	ds_read2_b32 v[146:147], v214 offset1:1
	v_readlane_b32 s100, v254, 59
	s_nop 1
	v_mov_b32_e32 v214, s100
	ds_read2_b32 v[148:149], v214 offset1:1
	v_readlane_b32 s100, v254, 60
	s_nop 1
	v_mov_b32_e32 v214, s100
	ds_read2_b32 v[150:151], v214 offset1:1
	v_readlane_b32 s100, v254, 62
	s_nop 1
	v_mov_b32_e32 v214, s100
	ds_read2_b32 v[152:153], v214 offset1:1
	v_readlane_b32 s100, v254, 63
	s_nop 1
	v_mov_b32_e32 v214, s100
	ds_read2_b32 v[154:155], v214 offset1:1
	v_readlane_b32 s100, v255, 1
	s_nop 1
	v_mov_b32_e32 v214, s100
	ds_read2_b32 v[156:157], v214 offset1:1
	s_waitcnt lgkmcnt(0)
	v_mov_b32_e32 v0, v128
	v_mov_b32_e32 v1, v129
	v_readlane_b32 s16, v254, 45
	s_waitcnt lgkmcnt(0)
	v_cmp_ge_i32_e32 vcc, s23, v0
	s_nop 1
	v_cndmask_b32_e64 v0, 0, 1, vcc
	v_cmp_lt_i32_e32 vcc, s23, v1
	s_nop 1
	v_cndmask_b32_e32 v2, 2, v0, vcc
	v_mov_b32_e32 v0, v130
	v_mov_b32_e32 v1, v131
	v_readlane_b32 s16, v254, 47
	s_waitcnt lgkmcnt(0)
	v_cmp_lt_i32_e32 vcc, s23, v0
	s_nop 1
	v_cndmask_b32_e32 v0, 3, v2, vcc
	v_cmp_lt_i32_e32 vcc, s23, v1
	s_nop 1
	v_cndmask_b32_e32 v2, 4, v0, vcc
	v_mov_b32_e32 v0, v132
	v_mov_b32_e32 v1, v133
	v_readlane_b32 s16, v254, 48
	s_waitcnt lgkmcnt(0)
	v_cmp_lt_i32_e32 vcc, s23, v0
	s_nop 1
	v_cndmask_b32_e32 v0, 5, v2, vcc
	v_cmp_lt_i32_e32 vcc, s23, v1
	s_nop 1
	v_cndmask_b32_e32 v2, 6, v0, vcc
	v_mov_b32_e32 v0, v134
	v_mov_b32_e32 v1, v135
	v_readlane_b32 s16, v254, 50
	s_waitcnt lgkmcnt(0)
	v_cmp_lt_i32_e32 vcc, s23, v0
	s_nop 1
	v_cndmask_b32_e32 v0, 7, v2, vcc
	v_cmp_lt_i32_e32 vcc, s23, v1
	s_nop 1
	v_cndmask_b32_e32 v2, 8, v0, vcc
	v_mov_b32_e32 v0, v136
	v_mov_b32_e32 v1, v137
	v_readlane_b32 s16, v254, 51
	s_waitcnt lgkmcnt(0)
	v_cmp_lt_i32_e32 vcc, s23, v0
	s_nop 1
	v_cndmask_b32_e32 v0, 9, v2, vcc
	v_cmp_lt_i32_e32 vcc, s23, v1
	s_nop 1
	v_cndmask_b32_e32 v2, 10, v0, vcc
	v_mov_b32_e32 v0, v138
	v_mov_b32_e32 v1, v139
	v_readlane_b32 s16, v254, 53
	s_waitcnt lgkmcnt(0)
	v_cmp_lt_i32_e32 vcc, s23, v0
	s_nop 1
	v_cndmask_b32_e32 v0, 11, v2, vcc
	v_cmp_lt_i32_e32 vcc, s23, v1
	s_nop 1
	v_cndmask_b32_e32 v2, 12, v0, vcc
	v_mov_b32_e32 v0, v140
	v_mov_b32_e32 v1, v141
	v_readlane_b32 s16, v254, 54
	s_waitcnt lgkmcnt(0)
	v_cmp_lt_i32_e32 vcc, s23, v0
	s_nop 1
	v_cndmask_b32_e32 v0, 13, v2, vcc
	v_cmp_lt_i32_e32 vcc, s23, v1
	s_nop 1
	v_cndmask_b32_e32 v2, 14, v0, vcc
	v_mov_b32_e32 v0, v142
	v_mov_b32_e32 v1, v143
	v_readlane_b32 s16, v254, 56
	s_waitcnt lgkmcnt(0)
	v_cmp_lt_i32_e32 vcc, s23, v0
	s_nop 1
	v_cndmask_b32_e32 v0, 15, v2, vcc
	v_cmp_lt_i32_e32 vcc, s23, v1
	s_nop 1
	v_cndmask_b32_e32 v2, 16, v0, vcc
	v_mov_b32_e32 v0, v144
	v_mov_b32_e32 v1, v145
	v_readlane_b32 s16, v254, 57
	s_waitcnt lgkmcnt(0)
	v_cmp_lt_i32_e32 vcc, s23, v0
	s_nop 1
	v_cndmask_b32_e32 v0, 17, v2, vcc
	v_cmp_lt_i32_e32 vcc, s23, v1
	s_nop 1
	v_cndmask_b32_e32 v2, 18, v0, vcc
	v_mov_b32_e32 v0, v146
	v_mov_b32_e32 v1, v147
	v_readlane_b32 s16, v254, 59
	s_waitcnt lgkmcnt(0)
	v_cmp_lt_i32_e32 vcc, s23, v0
	s_nop 1
	v_cndmask_b32_e32 v0, 19, v2, vcc
	v_cmp_lt_i32_e32 vcc, s23, v1
	s_nop 1
	v_cndmask_b32_e32 v2, 20, v0, vcc
	v_mov_b32_e32 v0, v148
	v_mov_b32_e32 v1, v149
	v_readlane_b32 s16, v254, 60
	s_waitcnt lgkmcnt(0)
	v_cmp_lt_i32_e32 vcc, s23, v0
	s_nop 1
	v_cndmask_b32_e32 v0, 21, v2, vcc
	v_cmp_lt_i32_e32 vcc, s23, v1
	s_nop 1
	v_cndmask_b32_e32 v2, 22, v0, vcc
	v_mov_b32_e32 v0, v150
	v_mov_b32_e32 v1, v151
	v_readlane_b32 s16, v254, 62
	s_waitcnt lgkmcnt(0)
	v_cmp_lt_i32_e32 vcc, s23, v0
	s_nop 1
	v_cndmask_b32_e32 v0, 23, v2, vcc
	v_cmp_lt_i32_e32 vcc, s23, v1
	s_nop 1
	v_cndmask_b32_e32 v2, 24, v0, vcc
	v_mov_b32_e32 v0, v152
	v_mov_b32_e32 v1, v153
	v_readlane_b32 s16, v254, 63
	s_waitcnt lgkmcnt(0)
	v_cmp_lt_i32_e32 vcc, s23, v0
	s_nop 1
	v_cndmask_b32_e32 v0, 25, v2, vcc
	v_cmp_lt_i32_e32 vcc, s23, v1
	s_nop 1
	v_cndmask_b32_e32 v2, 26, v0, vcc
	v_mov_b32_e32 v0, v154
	v_mov_b32_e32 v1, v155
	v_readlane_b32 s16, v255, 1
	s_waitcnt lgkmcnt(0)
	v_cmp_lt_i32_e32 vcc, s23, v0
	s_nop 1
	v_cndmask_b32_e32 v0, 27, v2, vcc
	v_cmp_lt_i32_e32 vcc, s23, v1
	s_nop 1
	v_cndmask_b32_e32 v2, 28, v0, vcc
	v_mov_b32_e32 v0, v156
	v_mov_b32_e32 v1, v157
	v_readlane_b32 s16, v255, 2
	s_waitcnt lgkmcnt(0)
	v_cmp_lt_i32_e32 vcc, s23, v0
	s_nop 1
	v_cndmask_b32_e32 v0, 29, v2, vcc
	v_cmp_lt_i32_e32 vcc, s23, v1
	v_mov_b32_e32 v1, s16
	ds_read_b32 v1, v1
	v_cndmask_b32_e32 v0, 30, v0, vcc
	s_waitcnt lgkmcnt(0)
	v_cmp_lt_i32_e32 vcc, s23, v1
	s_nop 1
	v_cndmask_b32_e32 v0, 31, v0, vcc
	v_lshlrev_b32_e32 v1, 2, v0
	v_add_u32_e32 v1, 0, v1
	v_add_u32_e32 v2, 0x24000, v1
	ds_read_b32 v2, v2
	v_add_u32_e32 v1, 0x24100, v1
	ds_read_b32 v1, v1
	s_waitcnt lgkmcnt(1)
	v_readfirstlane_b32 s16, v2
	s_addk_i32 s16, 0xff
	s_ashr_i32 s16, s16, 8
	s_abs_i32 s20, s16
	s_waitcnt lgkmcnt(0)
	v_readfirstlane_b32 s17, v1
	v_cvt_f32_u32_e32 v1, s20
	s_sub_i32 s21, 0, s20
	s_sub_i32 s17, s23, s17
	s_abs_i32 s19, s17
	v_rcp_iflag_f32_e32 v1, v1
	s_xor_b32 s18, s17, s16
	s_ashr_i32 s18, s18, 31
	v_mul_f32_e32 v1, 0x4f7ffffe, v1
	v_cvt_u32_f32_e32 v1, v1
	s_nop 0
	v_readfirstlane_b32 s24, v1
	s_mul_i32 s21, s21, s24
	s_mul_hi_u32 s21, s24, s21
	s_add_i32 s24, s24, s21
	s_mul_hi_u32 s21, s19, s24
	s_mul_i32 s24, s21, s20
	s_sub_i32 s19, s19, s24
	s_add_i32 s24, s21, 1
	s_sub_i32 s25, s19, s20
	s_cmp_ge_u32 s19, s20
	s_cselect_b32 s21, s24, s21
	s_cselect_b32 s19, s25, s19
	s_add_i32 s24, s21, 1
	s_cmp_ge_u32 s19, s20
	s_cselect_b32 s19, s24, s21
	s_xor_b32 s19, s19, s18
	s_sub_i32 s18, s19, s18
	s_mul_i32 s16, s18, s16
	s_sub_i32 s19, s17, s16
	v_lshl_add_u32 v1, s19, 8, v206
	v_cmp_lt_i32_e32 vcc, v1, v2
	s_and_saveexec_b64 s[16:17], vcc
	s_cbranch_execz .LBB0_1082
	v_lshl_add_u32 v2, v0, 13, v1
	v_ashrrev_i32_e32 v3, 31, v2
	v_lshl_add_u64 v[2:3], v[2:3], 2, s[14:15]
	global_load_dword v208, v[2:3], off

.LBB0_1087:
	v_cndmask_b32_e64 v0, 0, 1, s[6:7]
	v_cmp_ne_u32_e64 s[4:5], 1, v0
	s_andn2_b64 vcc, exec, s[6:7]
	s_cbranch_vccnz .LBB0_1097
	v_readlane_b32 s6, v255, 3
	s_add_i32 s16, s23, s22
	s_nop 0
	v_mov_b32_e32 v0, s6
	ds_read_b32 v0, v0
	s_waitcnt lgkmcnt(0)
	v_cmp_ge_i32_e32 vcc, s16, v0
	s_cbranch_vccnz .LBB0_1097
	s_movk_i32 s6, 0x100
	v_cmp_gt_i32_e32 vcc, s6, v206
	s_and_saveexec_b64 s[6:7], vcc
	s_cbranch_execz .LBB0_1096
	v_readlane_b32 s17, v255, 4
	v_mov_b32_e32 v208, -1
	s_nop 0
	v_readlane_b32 s100, v255, 4
	s_nop 1
	v_mov_b32_e32 v214, s100
	ds_read2_b32 v[128:129], v214 offset1:1
	v_readlane_b32 s100, v254, 45
	s_nop 1
	v_mov_b32_e32 v214, s100
	ds_read2_b32 v[130:131], v214 offset1:1
	v_readlane_b32 s100, v254, 47
	s_nop 1
	v_mov_b32_e32 v214, s100
	ds_read2_b32 v[132:133], v214 offset1:1
	v_readlane_b32 s100, v254, 48
	s_nop 1
	v_mov_b32_e32 v214, s100
	ds_read2_b32 v[134:135], v214 offset1:1
	v_readlane_b32 s100, v254, 50
	s_nop 1
	v_mov_b32_e32 v214, s100
	ds_read2_b32 v[136:137], v214 offset1:1
	v_readlane_b32 s100, v254, 51
	s_nop 1
	v_mov_b32_e32 v214, s100
	ds_read2_b32 v[138:139], v214 offset1:1
	v_readlane_b32 s100, v254, 53
	s_nop 1
	v_mov_b32_e32 v214, s100
	ds_read2_b32 v[140:141], v214 offset1:1
	v_readlane_b32 s100, v254, 54
	s_nop 1
	v_mov_b32_e32 v214, s100
	ds_read2_b32 v[142:143], v214 offset1:1
	s_waitcnt lgkmcnt(0)
	v_readlane_b32 s100, v254, 56
	s_nop 1
	v_mov_b32_e32 v214, s100
	ds_read2_b32 v[144:145], v214 offset1:1
	v_readlane_b32 s100, v254, 57
	s_nop 1
	v_mov_b32_e32 v214, s100
	ds_read2_b32 v[146:147], v214 offset1:1
	v_readlane_b32 s100, v254, 59
	s_nop 1
	v_mov_b32_e32 v214, s100
	ds_read2_b32 v[148:149], v214 offset1:1
	v_readlane_b32 s100, v254, 60
	s_nop 1
	v_mov_b32_e32 v214, s100
	ds_read2_b32 v[150:151], v214 offset1:1
	v_readlane_b32 s100, v254, 62
	s_nop 1
	v_mov_b32_e32 v214, s100
	ds_read2_b32 v[152:153], v214 offset1:1
	v_readlane_b32 s100, v254, 63
	s_nop 1
	v_mov_b32_e32 v214, s100
	ds_read2_b32 v[154:155], v214 offset1:1
	v_readlane_b32 s100, v255, 1
	s_nop 1
	v_mov_b32_e32 v214, s100
	ds_read2_b32 v[156:157], v214 offset1:1
	s_waitcnt lgkmcnt(0)
	v_mov_b32_e32 v0, v128
	v_mov_b32_e32 v1, v129
	v_readlane_b32 s17, v254, 45
	s_waitcnt lgkmcnt(0)
	v_cmp_ge_i32_e32 vcc, s16, v0
	s_nop 1
	v_cndmask_b32_e64 v0, 0, 1, vcc
	v_cmp_lt_i32_e32 vcc, s16, v1
	s_nop 1
	v_cndmask_b32_e32 v2, 2, v0, vcc
	v_mov_b32_e32 v0, v130
	v_mov_b32_e32 v1, v131
	v_readlane_b32 s17, v254, 47
	s_waitcnt lgkmcnt(0)
	v_cmp_lt_i32_e32 vcc, s16, v0
	s_nop 1
	v_cndmask_b32_e32 v0, 3, v2, vcc
	v_cmp_lt_i32_e32 vcc, s16, v1
	s_nop 1
	v_cndmask_b32_e32 v2, 4, v0, vcc
	v_mov_b32_e32 v0, v132
	v_mov_b32_e32 v1, v133
	v_readlane_b32 s17, v254, 48
	s_waitcnt lgkmcnt(0)
	v_cmp_lt_i32_e32 vcc, s16, v0
	s_nop 1
	v_cndmask_b32_e32 v0, 5, v2, vcc
	v_cmp_lt_i32_e32 vcc, s16, v1
	s_nop 1
	v_cndmask_b32_e32 v2, 6, v0, vcc
	v_mov_b32_e32 v0, v134
	v_mov_b32_e32 v1, v135
	v_readlane_b32 s17, v254, 50
	s_waitcnt lgkmcnt(0)
	v_cmp_lt_i32_e32 vcc, s16, v0
	s_nop 1
	v_cndmask_b32_e32 v0, 7, v2, vcc
	v_cmp_lt_i32_e32 vcc, s16, v1
	s_nop 1
	v_cndmask_b32_e32 v2, 8, v0, vcc
	v_mov_b32_e32 v0, v136
	v_mov_b32_e32 v1, v137
	v_readlane_b32 s17, v254, 51
	s_waitcnt lgkmcnt(0)
	v_cmp_lt_i32_e32 vcc, s16, v0
	s_nop 1
	v_cndmask_b32_e32 v0, 9, v2, vcc
	v_cmp_lt_i32_e32 vcc, s16, v1
	s_nop 1
	v_cndmask_b32_e32 v2, 10, v0, vcc
	v_mov_b32_e32 v0, v138
	v_mov_b32_e32 v1, v139
	v_readlane_b32 s17, v254, 53
	s_waitcnt lgkmcnt(0)
	v_cmp_lt_i32_e32 vcc, s16, v0
	s_nop 1
	v_cndmask_b32_e32 v0, 11, v2, vcc
	v_cmp_lt_i32_e32 vcc, s16, v1
	s_nop 1
	v_cndmask_b32_e32 v2, 12, v0, vcc
	v_mov_b32_e32 v0, v140
	v_mov_b32_e32 v1, v141
	v_readlane_b32 s17, v254, 54
	s_waitcnt lgkmcnt(0)
	v_cmp_lt_i32_e32 vcc, s16, v0
	s_nop 1
	v_cndmask_b32_e32 v0, 13, v2, vcc
	v_cmp_lt_i32_e32 vcc, s16, v1
	s_nop 1
	v_cndmask_b32_e32 v2, 14, v0, vcc
	v_mov_b32_e32 v0, v142
	v_mov_b32_e32 v1, v143
	v_readlane_b32 s17, v254, 56
	s_waitcnt lgkmcnt(0)
	v_cmp_lt_i32_e32 vcc, s16, v0
	s_nop 1
	v_cndmask_b32_e32 v0, 15, v2, vcc
	v_cmp_lt_i32_e32 vcc, s16, v1
	s_nop 1
	v_cndmask_b32_e32 v2, 16, v0, vcc
	v_mov_b32_e32 v0, v144
	v_mov_b32_e32 v1, v145
	v_readlane_b32 s17, v254, 57
	s_waitcnt lgkmcnt(0)
	v_cmp_lt_i32_e32 vcc, s16, v0
	s_nop 1
	v_cndmask_b32_e32 v0, 17, v2, vcc
	v_cmp_lt_i32_e32 vcc, s16, v1
	s_nop 1
	v_cndmask_b32_e32 v2, 18, v0, vcc
	v_mov_b32_e32 v0, v146
	v_mov_b32_e32 v1, v147
	v_readlane_b32 s17, v254, 59
	s_waitcnt lgkmcnt(0)
	v_cmp_lt_i32_e32 vcc, s16, v0
	s_nop 1
	v_cndmask_b32_e32 v0, 19, v2, vcc
	v_cmp_lt_i32_e32 vcc, s16, v1
	s_nop 1
	v_cndmask_b32_e32 v2, 20, v0, vcc
	v_mov_b32_e32 v0, v148
	v_mov_b32_e32 v1, v149
	v_readlane_b32 s17, v254, 60
	s_waitcnt lgkmcnt(0)
	v_cmp_lt_i32_e32 vcc, s16, v0
	s_nop 1
	v_cndmask_b32_e32 v0, 21, v2, vcc
	v_cmp_lt_i32_e32 vcc, s16, v1
	s_nop 1
	v_cndmask_b32_e32 v2, 22, v0, vcc
	v_mov_b32_e32 v0, v150
	v_mov_b32_e32 v1, v151
	v_readlane_b32 s17, v254, 62
	s_waitcnt lgkmcnt(0)
	v_cmp_lt_i32_e32 vcc, s16, v0
	s_nop 1
	v_cndmask_b32_e32 v0, 23, v2, vcc
	v_cmp_lt_i32_e32 vcc, s16, v1
	s_nop 1
	v_cndmask_b32_e32 v2, 24, v0, vcc
	v_mov_b32_e32 v0, v152
	v_mov_b32_e32 v1, v153
	v_readlane_b32 s17, v254, 63
	s_waitcnt lgkmcnt(0)
	v_cmp_lt_i32_e32 vcc, s16, v0
	s_nop 1
	v_cndmask_b32_e32 v0, 25, v2, vcc
	v_cmp_lt_i32_e32 vcc, s16, v1
	s_nop 1
	v_cndmask_b32_e32 v2, 26, v0, vcc
	v_mov_b32_e32 v0, v154
	v_mov_b32_e32 v1, v155
	v_readlane_b32 s17, v255, 1
	s_waitcnt lgkmcnt(0)
	v_cmp_lt_i32_e32 vcc, s16, v0
	s_nop 1
	v_cndmask_b32_e32 v0, 27, v2, vcc
	v_cmp_lt_i32_e32 vcc, s16, v1
	s_nop 1
	v_cndmask_b32_e32 v2, 28, v0, vcc
	v_mov_b32_e32 v0, v156
	v_mov_b32_e32 v1, v157
	v_readlane_b32 s17, v255, 2
	s_waitcnt lgkmcnt(0)
	v_cmp_lt_i32_e32 vcc, s16, v0
	s_nop 1
	v_cndmask_b32_e32 v0, 29, v2, vcc
	v_cmp_lt_i32_e32 vcc, s16, v1
	v_mov_b32_e32 v1, s17
	ds_read_b32 v1, v1
	v_cndmask_b32_e32 v0, 30, v0, vcc
	s_waitcnt lgkmcnt(0)
	v_cmp_lt_i32_e32 vcc, s16, v1
	s_nop 1
	v_cndmask_b32_e32 v0, 31, v0, vcc
	v_lshlrev_b32_e32 v1, 2, v0
	v_add_u32_e32 v1, 0, v1
	v_add_u32_e32 v2, 0x24000, v1
	ds_read_b32 v2, v2
	v_add_u32_e32 v1, 0x24100, v1
	ds_read_b32 v1, v1
	s_waitcnt lgkmcnt(1)
	v_readfirstlane_b32 s17, v2
	s_addk_i32 s17, 0xff
	s_ashr_i32 s17, s17, 8
	s_abs_i32 s21, s17
	s_waitcnt lgkmcnt(0)
	v_readfirstlane_b32 s19, v1
	v_cvt_f32_u32_e32 v1, s21
	s_sub_i32 s24, 0, s21
	s_sub_i32 s16, s16, s19
	s_abs_i32 s20, s16
	v_rcp_iflag_f32_e32 v1, v1
	s_xor_b32 s19, s16, s17
	s_ashr_i32 s19, s19, 31
	v_mul_f32_e32 v1, 0x4f7ffffe, v1
	v_cvt_u32_f32_e32 v1, v1
	s_nop 0
	v_readfirstlane_b32 s25, v1
	s_mul_i32 s24, s24, s25
	s_mul_hi_u32 s24, s25, s24
	s_add_i32 s25, s25, s24
	s_mul_hi_u32 s24, s20, s25
	s_mul_i32 s25, s24, s21
	s_sub_i32 s20, s20, s25
	s_add_i32 s25, s24, 1
	s_sub_i32 s26, s20, s21
	s_cmp_ge_u32 s20, s21
	s_cselect_b32 s24, s25, s24
	s_cselect_b32 s20, s26, s20
	s_add_i32 s25, s24, 1
	s_cmp_ge_u32 s20, s21
	s_cselect_b32 s20, s25, s24
	s_xor_b32 s20, s20, s19
	s_sub_i32 s19, s20, s19
	s_mul_i32 s17, s19, s17
	s_sub_i32 s20, s16, s17
	v_lshl_add_u32 v1, s20, 8, v206
	v_cmp_lt_i32_e32 vcc, v1, v2
	s_and_saveexec_b64 s[16:17], vcc
	s_cbranch_execz .LBB0_1092
	v_lshl_add_u32 v2, v0, 13, v1
	v_ashrrev_i32_e32 v3, 31, v2
	v_lshl_add_u64 v[2:3], v[2:3], 2, s[14:15]
	global_load_dword v208, v[2:3], off

.LBB0_1097:
	s_and_b64 vcc, exec, s[4:5]
	s_cbranch_vccnz .LBB0_1107
	v_readlane_b32 s6, v255, 3
	s_nop 1
	v_mov_b32_e32 v0, s6
	ds_read_b32 v0, v0
	s_lshl_b32 s6, s22, 1
	s_add_i32 s16, s23, s6
	s_waitcnt lgkmcnt(0)
	v_cmp_ge_i32_e32 vcc, s16, v0
	s_cbranch_vccnz .LBB0_1107
	s_movk_i32 s6, 0x100
	v_cmp_gt_i32_e32 vcc, s6, v206
	s_and_saveexec_b64 s[6:7], vcc
	s_cbranch_execz .LBB0_1106
	v_readlane_b32 s17, v255, 4
	v_mov_b32_e32 v208, -1
	s_nop 0
	v_readlane_b32 s100, v255, 4
	s_nop 1
	v_mov_b32_e32 v214, s100
	ds_read2_b32 v[128:129], v214 offset1:1
	v_readlane_b32 s100, v254, 45
	s_nop 1
	v_mov_b32_e32 v214, s100
	ds_read2_b32 v[130:131], v214 offset1:1
	v_readlane_b32 s100, v254, 47
	s_nop 1
	v_mov_b32_e32 v214, s100
	ds_read2_b32 v[132:133], v214 offset1:1
	v_readlane_b32 s100, v254, 48
	s_nop 1
	v_mov_b32_e32 v214, s100
	ds_read2_b32 v[134:135], v214 offset1:1
	v_readlane_b32 s100, v254, 50
	s_nop 1
	v_mov_b32_e32 v214, s100
	ds_read2_b32 v[136:137], v214 offset1:1
	v_readlane_b32 s100, v254, 51
	s_nop 1
	v_mov_b32_e32 v214, s100
	ds_read2_b32 v[138:139], v214 offset1:1
	v_readlane_b32 s100, v254, 53
	s_nop 1
	v_mov_b32_e32 v214, s100
	ds_read2_b32 v[140:141], v214 offset1:1
	v_readlane_b32 s100, v254, 54
	s_nop 1
	v_mov_b32_e32 v214, s100
	ds_read2_b32 v[142:143], v214 offset1:1
	s_waitcnt lgkmcnt(0)
	v_readlane_b32 s100, v254, 56
	s_nop 1
	v_mov_b32_e32 v214, s100
	ds_read2_b32 v[144:145], v214 offset1:1
	v_readlane_b32 s100, v254, 57
	s_nop 1
	v_mov_b32_e32 v214, s100
	ds_read2_b32 v[146:147], v214 offset1:1
	v_readlane_b32 s100, v254, 59
	s_nop 1
	v_mov_b32_e32 v214, s100
	ds_read2_b32 v[148:149], v214 offset1:1
	v_readlane_b32 s100, v254, 60
	s_nop 1
	v_mov_b32_e32 v214, s100
	ds_read2_b32 v[150:151], v214 offset1:1
	v_readlane_b32 s100, v254, 62
	s_nop 1
	v_mov_b32_e32 v214, s100
	ds_read2_b32 v[152:153], v214 offset1:1
	v_readlane_b32 s100, v254, 63
	s_nop 1
	v_mov_b32_e32 v214, s100
	ds_read2_b32 v[154:155], v214 offset1:1
	v_readlane_b32 s100, v255, 1
	s_nop 1
	v_mov_b32_e32 v214, s100
	ds_read2_b32 v[156:157], v214 offset1:1
	s_waitcnt lgkmcnt(0)
	v_mov_b32_e32 v0, v128
	v_mov_b32_e32 v1, v129
	v_readlane_b32 s17, v254, 45
	s_waitcnt lgkmcnt(0)
	v_cmp_ge_i32_e32 vcc, s16, v0
	s_nop 1
	v_cndmask_b32_e64 v0, 0, 1, vcc
	v_cmp_lt_i32_e32 vcc, s16, v1
	s_nop 1
	v_cndmask_b32_e32 v2, 2, v0, vcc
	v_mov_b32_e32 v0, v130
	v_mov_b32_e32 v1, v131
	v_readlane_b32 s17, v254, 47
	s_waitcnt lgkmcnt(0)
	v_cmp_lt_i32_e32 vcc, s16, v0
	s_nop 1
	v_cndmask_b32_e32 v0, 3, v2, vcc
	v_cmp_lt_i32_e32 vcc, s16, v1
	s_nop 1
	v_cndmask_b32_e32 v2, 4, v0, vcc
	v_mov_b32_e32 v0, v132
	v_mov_b32_e32 v1, v133
	v_readlane_b32 s17, v254, 48
	s_waitcnt lgkmcnt(0)
	v_cmp_lt_i32_e32 vcc, s16, v0
	s_nop 1
	v_cndmask_b32_e32 v0, 5, v2, vcc
	v_cmp_lt_i32_e32 vcc, s16, v1
	s_nop 1
	v_cndmask_b32_e32 v2, 6, v0, vcc
	v_mov_b32_e32 v0, v134
	v_mov_b32_e32 v1, v135
	v_readlane_b32 s17, v254, 50
	s_waitcnt lgkmcnt(0)
	v_cmp_lt_i32_e32 vcc, s16, v0
	s_nop 1
	v_cndmask_b32_e32 v0, 7, v2, vcc
	v_cmp_lt_i32_e32 vcc, s16, v1
	s_nop 1
	v_cndmask_b32_e32 v2, 8, v0, vcc
	v_mov_b32_e32 v0, v136
	v_mov_b32_e32 v1, v137
	v_readlane_b32 s17, v254, 51
	s_waitcnt lgkmcnt(0)
	v_cmp_lt_i32_e32 vcc, s16, v0
	s_nop 1
	v_cndmask_b32_e32 v0, 9, v2, vcc
	v_cmp_lt_i32_e32 vcc, s16, v1
	s_nop 1
	v_cndmask_b32_e32 v2, 10, v0, vcc
	v_mov_b32_e32 v0, v138
	v_mov_b32_e32 v1, v139
	v_readlane_b32 s17, v254, 53
	s_waitcnt lgkmcnt(0)
	v_cmp_lt_i32_e32 vcc, s16, v0
	s_nop 1
	v_cndmask_b32_e32 v0, 11, v2, vcc
	v_cmp_lt_i32_e32 vcc, s16, v1
	s_nop 1
	v_cndmask_b32_e32 v2, 12, v0, vcc
	v_mov_b32_e32 v0, v140
	v_mov_b32_e32 v1, v141
	v_readlane_b32 s17, v254, 54
	s_waitcnt lgkmcnt(0)
	v_cmp_lt_i32_e32 vcc, s16, v0
	s_nop 1
	v_cndmask_b32_e32 v0, 13, v2, vcc
	v_cmp_lt_i32_e32 vcc, s16, v1
	s_nop 1
	v_cndmask_b32_e32 v2, 14, v0, vcc
	v_mov_b32_e32 v0, v142
	v_mov_b32_e32 v1, v143
	v_readlane_b32 s17, v254, 56
	s_waitcnt lgkmcnt(0)
	v_cmp_lt_i32_e32 vcc, s16, v0
	s_nop 1
	v_cndmask_b32_e32 v0, 15, v2, vcc
	v_cmp_lt_i32_e32 vcc, s16, v1
	s_nop 1
	v_cndmask_b32_e32 v2, 16, v0, vcc
	v_mov_b32_e32 v0, v144
	v_mov_b32_e32 v1, v145
	v_readlane_b32 s17, v254, 57
	s_waitcnt lgkmcnt(0)
	v_cmp_lt_i32_e32 vcc, s16, v0
	s_nop 1
	v_cndmask_b32_e32 v0, 17, v2, vcc
	v_cmp_lt_i32_e32 vcc, s16, v1
	s_nop 1
	v_cndmask_b32_e32 v2, 18, v0, vcc
	v_mov_b32_e32 v0, v146
	v_mov_b32_e32 v1, v147
	v_readlane_b32 s17, v254, 59
	s_waitcnt lgkmcnt(0)
	v_cmp_lt_i32_e32 vcc, s16, v0
	s_nop 1
	v_cndmask_b32_e32 v0, 19, v2, vcc
	v_cmp_lt_i32_e32 vcc, s16, v1
	s_nop 1
	v_cndmask_b32_e32 v2, 20, v0, vcc
	v_mov_b32_e32 v0, v148
	v_mov_b32_e32 v1, v149
	v_readlane_b32 s17, v254, 60
	s_waitcnt lgkmcnt(0)
	v_cmp_lt_i32_e32 vcc, s16, v0
	s_nop 1
	v_cndmask_b32_e32 v0, 21, v2, vcc
	v_cmp_lt_i32_e32 vcc, s16, v1
	s_nop 1
	v_cndmask_b32_e32 v2, 22, v0, vcc
	v_mov_b32_e32 v0, v150
	v_mov_b32_e32 v1, v151
	v_readlane_b32 s17, v254, 62
	s_waitcnt lgkmcnt(0)
	v_cmp_lt_i32_e32 vcc, s16, v0
	s_nop 1
	v_cndmask_b32_e32 v0, 23, v2, vcc
	v_cmp_lt_i32_e32 vcc, s16, v1
	s_nop 1
	v_cndmask_b32_e32 v2, 24, v0, vcc
	v_mov_b32_e32 v0, v152
	v_mov_b32_e32 v1, v153
	v_readlane_b32 s17, v254, 63
	s_waitcnt lgkmcnt(0)
	v_cmp_lt_i32_e32 vcc, s16, v0
	s_nop 1
	v_cndmask_b32_e32 v0, 25, v2, vcc
	v_cmp_lt_i32_e32 vcc, s16, v1
	s_nop 1
	v_cndmask_b32_e32 v2, 26, v0, vcc
	v_mov_b32_e32 v0, v154
	v_mov_b32_e32 v1, v155
	v_readlane_b32 s17, v255, 1
	s_waitcnt lgkmcnt(0)
	v_cmp_lt_i32_e32 vcc, s16, v0
	s_nop 1
	v_cndmask_b32_e32 v0, 27, v2, vcc
	v_cmp_lt_i32_e32 vcc, s16, v1
	s_nop 1
	v_cndmask_b32_e32 v2, 28, v0, vcc
	v_mov_b32_e32 v0, v156
	v_mov_b32_e32 v1, v157
	v_readlane_b32 s17, v255, 2
	s_waitcnt lgkmcnt(0)
	v_cmp_lt_i32_e32 vcc, s16, v0
	s_nop 1
	v_cndmask_b32_e32 v0, 29, v2, vcc
	v_cmp_lt_i32_e32 vcc, s16, v1
	v_mov_b32_e32 v1, s17
	ds_read_b32 v1, v1
	v_cndmask_b32_e32 v0, 30, v0, vcc
	s_waitcnt lgkmcnt(0)
	v_cmp_lt_i32_e32 vcc, s16, v1
	s_nop 1
	v_cndmask_b32_e32 v0, 31, v0, vcc
	v_lshlrev_b32_e32 v1, 2, v0
	v_add_u32_e32 v1, 0, v1
	v_add_u32_e32 v2, 0x24000, v1
	ds_read_b32 v2, v2
	v_add_u32_e32 v1, 0x24100, v1
	ds_read_b32 v1, v1
	s_waitcnt lgkmcnt(1)
	v_readfirstlane_b32 s17, v2
	s_addk_i32 s17, 0xff
	s_ashr_i32 s17, s17, 8
	s_abs_i32 s21, s17
	s_waitcnt lgkmcnt(0)
	v_readfirstlane_b32 s19, v1
	v_cvt_f32_u32_e32 v1, s21
	s_sub_i32 s24, 0, s21
	s_sub_i32 s16, s16, s19
	s_abs_i32 s20, s16
	v_rcp_iflag_f32_e32 v1, v1
	s_xor_b32 s19, s16, s17
	s_ashr_i32 s19, s19, 31
	v_mul_f32_e32 v1, 0x4f7ffffe, v1
	v_cvt_u32_f32_e32 v1, v1
	s_nop 0
	v_readfirstlane_b32 s25, v1
	s_mul_i32 s24, s24, s25
	s_mul_hi_u32 s24, s25, s24
	s_add_i32 s25, s25, s24
	s_mul_hi_u32 s24, s20, s25
	s_mul_i32 s25, s24, s21
	s_sub_i32 s20, s20, s25
	s_add_i32 s25, s24, 1
	s_sub_i32 s26, s20, s21
	s_cmp_ge_u32 s20, s21
	s_cselect_b32 s24, s25, s24
	s_cselect_b32 s20, s26, s20
	s_add_i32 s25, s24, 1
	s_cmp_ge_u32 s20, s21
	s_cselect_b32 s20, s25, s24
	s_xor_b32 s20, s20, s19
	s_sub_i32 s19, s20, s19
	s_mul_i32 s17, s19, s17
	s_sub_i32 s20, s16, s17
	v_lshl_add_u32 v1, s20, 8, v206
	v_cmp_lt_i32_e32 vcc, v1, v2
	s_and_saveexec_b64 s[16:17], vcc
	s_cbranch_execz .LBB0_1102
	v_lshl_add_u32 v2, v0, 13, v1
	v_ashrrev_i32_e32 v3, 31, v2
	v_lshl_add_u64 v[2:3], v[2:3], 2, s[14:15]
	global_load_dword v208, v[2:3], off

.LBB0_1107:
	s_and_b64 vcc, exec, s[4:5]
	s_cbranch_vccnz .LBB0_1117
	v_readlane_b32 s6, v255, 3
	s_nop 1
	v_mov_b32_e32 v0, s6
	ds_read_b32 v0, v0
	s_mul_i32 s6, s22, 3
	s_add_i32 s16, s23, s6
	s_waitcnt lgkmcnt(0)
	v_cmp_ge_i32_e32 vcc, s16, v0
	s_cbranch_vccnz .LBB0_1117
	s_movk_i32 s6, 0x100
	v_cmp_gt_i32_e32 vcc, s6, v206
	s_and_saveexec_b64 s[6:7], vcc
	s_cbranch_execz .LBB0_1116
	v_readlane_b32 s17, v255, 4
	v_mov_b32_e32 v208, -1
	s_nop 0
	v_readlane_b32 s100, v255, 4
	s_nop 1
	v_mov_b32_e32 v214, s100
	ds_read2_b32 v[128:129], v214 offset1:1
	v_readlane_b32 s100, v254, 45
	s_nop 1
	v_mov_b32_e32 v214, s100
	ds_read2_b32 v[130:131], v214 offset1:1
	v_readlane_b32 s100, v254, 47
	s_nop 1
	v_mov_b32_e32 v214, s100
	ds_read2_b32 v[132:133], v214 offset1:1
	v_readlane_b32 s100, v254, 48
	s_nop 1
	v_mov_b32_e32 v214, s100
	ds_read2_b32 v[134:135], v214 offset1:1
	v_readlane_b32 s100, v254, 50
	s_nop 1
	v_mov_b32_e32 v214, s100
	ds_read2_b32 v[136:137], v214 offset1:1
	v_readlane_b32 s100, v254, 51
	s_nop 1
	v_mov_b32_e32 v214, s100
	ds_read2_b32 v[138:139], v214 offset1:1
	v_readlane_b32 s100, v254, 53
	s_nop 1
	v_mov_b32_e32 v214, s100
	ds_read2_b32 v[140:141], v214 offset1:1
	v_readlane_b32 s100, v254, 54
	s_nop 1
	v_mov_b32_e32 v214, s100
	ds_read2_b32 v[142:143], v214 offset1:1
	s_waitcnt lgkmcnt(0)
	v_readlane_b32 s100, v254, 56
	s_nop 1
	v_mov_b32_e32 v214, s100
	ds_read2_b32 v[144:145], v214 offset1:1
	v_readlane_b32 s100, v254, 57
	s_nop 1
	v_mov_b32_e32 v214, s100
	ds_read2_b32 v[146:147], v214 offset1:1
	v_readlane_b32 s100, v254, 59
	s_nop 1
	v_mov_b32_e32 v214, s100
	ds_read2_b32 v[148:149], v214 offset1:1
	v_readlane_b32 s100, v254, 60
	s_nop 1
	v_mov_b32_e32 v214, s100
	ds_read2_b32 v[150:151], v214 offset1:1
	v_readlane_b32 s100, v254, 62
	s_nop 1
	v_mov_b32_e32 v214, s100
	ds_read2_b32 v[152:153], v214 offset1:1
	v_readlane_b32 s100, v254, 63
	s_nop 1
	v_mov_b32_e32 v214, s100
	ds_read2_b32 v[154:155], v214 offset1:1
	v_readlane_b32 s100, v255, 1
	s_nop 1
	v_mov_b32_e32 v214, s100
	ds_read2_b32 v[156:157], v214 offset1:1
	s_waitcnt lgkmcnt(0)
	v_mov_b32_e32 v0, v128
	v_mov_b32_e32 v1, v129
	v_readlane_b32 s17, v254, 45
	s_waitcnt lgkmcnt(0)
	v_cmp_ge_i32_e32 vcc, s16, v0
	s_nop 1
	v_cndmask_b32_e64 v0, 0, 1, vcc
	v_cmp_lt_i32_e32 vcc, s16, v1
	s_nop 1
	v_cndmask_b32_e32 v2, 2, v0, vcc
	v_mov_b32_e32 v0, v130
	v_mov_b32_e32 v1, v131
	v_readlane_b32 s17, v254, 47
	s_waitcnt lgkmcnt(0)
	v_cmp_lt_i32_e32 vcc, s16, v0
	s_nop 1
	v_cndmask_b32_e32 v0, 3, v2, vcc
	v_cmp_lt_i32_e32 vcc, s16, v1
	s_nop 1
	v_cndmask_b32_e32 v2, 4, v0, vcc
	v_mov_b32_e32 v0, v132
	v_mov_b32_e32 v1, v133
	v_readlane_b32 s17, v254, 48
	s_waitcnt lgkmcnt(0)
	v_cmp_lt_i32_e32 vcc, s16, v0
	s_nop 1
	v_cndmask_b32_e32 v0, 5, v2, vcc
	v_cmp_lt_i32_e32 vcc, s16, v1
	s_nop 1
	v_cndmask_b32_e32 v2, 6, v0, vcc
	v_mov_b32_e32 v0, v134
	v_mov_b32_e32 v1, v135
	v_readlane_b32 s17, v254, 50
	s_waitcnt lgkmcnt(0)
	v_cmp_lt_i32_e32 vcc, s16, v0
	s_nop 1
	v_cndmask_b32_e32 v0, 7, v2, vcc
	v_cmp_lt_i32_e32 vcc, s16, v1
	s_nop 1
	v_cndmask_b32_e32 v2, 8, v0, vcc
	v_mov_b32_e32 v0, v136
	v_mov_b32_e32 v1, v137
	v_readlane_b32 s17, v254, 51
	s_waitcnt lgkmcnt(0)
	v_cmp_lt_i32_e32 vcc, s16, v0
	s_nop 1
	v_cndmask_b32_e32 v0, 9, v2, vcc
	v_cmp_lt_i32_e32 vcc, s16, v1
	s_nop 1
	v_cndmask_b32_e32 v2, 10, v0, vcc
	v_mov_b32_e32 v0, v138
	v_mov_b32_e32 v1, v139
	v_readlane_b32 s17, v254, 53
	s_waitcnt lgkmcnt(0)
	v_cmp_lt_i32_e32 vcc, s16, v0
	s_nop 1
	v_cndmask_b32_e32 v0, 11, v2, vcc
	v_cmp_lt_i32_e32 vcc, s16, v1
	s_nop 1
	v_cndmask_b32_e32 v2, 12, v0, vcc
	v_mov_b32_e32 v0, v140
	v_mov_b32_e32 v1, v141
	v_readlane_b32 s17, v254, 54
	s_waitcnt lgkmcnt(0)
	v_cmp_lt_i32_e32 vcc, s16, v0
	s_nop 1
	v_cndmask_b32_e32 v0, 13, v2, vcc
	v_cmp_lt_i32_e32 vcc, s16, v1
	s_nop 1
	v_cndmask_b32_e32 v2, 14, v0, vcc
	v_mov_b32_e32 v0, v142
	v_mov_b32_e32 v1, v143
	v_readlane_b32 s17, v254, 56
	s_waitcnt lgkmcnt(0)
	v_cmp_lt_i32_e32 vcc, s16, v0
	s_nop 1
	v_cndmask_b32_e32 v0, 15, v2, vcc
	v_cmp_lt_i32_e32 vcc, s16, v1
	s_nop 1
	v_cndmask_b32_e32 v2, 16, v0, vcc
	v_mov_b32_e32 v0, v144
	v_mov_b32_e32 v1, v145
	v_readlane_b32 s17, v254, 57
	s_waitcnt lgkmcnt(0)
	v_cmp_lt_i32_e32 vcc, s16, v0
	s_nop 1
	v_cndmask_b32_e32 v0, 17, v2, vcc
	v_cmp_lt_i32_e32 vcc, s16, v1
	s_nop 1
	v_cndmask_b32_e32 v2, 18, v0, vcc
	v_mov_b32_e32 v0, v146
	v_mov_b32_e32 v1, v147
	v_readlane_b32 s17, v254, 59
	s_waitcnt lgkmcnt(0)
	v_cmp_lt_i32_e32 vcc, s16, v0
	s_nop 1
	v_cndmask_b32_e32 v0, 19, v2, vcc
	v_cmp_lt_i32_e32 vcc, s16, v1
	s_nop 1
	v_cndmask_b32_e32 v2, 20, v0, vcc
	v_mov_b32_e32 v0, v148
	v_mov_b32_e32 v1, v149
	v_readlane_b32 s17, v254, 60
	s_waitcnt lgkmcnt(0)
	v_cmp_lt_i32_e32 vcc, s16, v0
	s_nop 1
	v_cndmask_b32_e32 v0, 21, v2, vcc
	v_cmp_lt_i32_e32 vcc, s16, v1
	s_nop 1
	v_cndmask_b32_e32 v2, 22, v0, vcc
	v_mov_b32_e32 v0, v150
	v_mov_b32_e32 v1, v151
	v_readlane_b32 s17, v254, 62
	s_waitcnt lgkmcnt(0)
	v_cmp_lt_i32_e32 vcc, s16, v0
	s_nop 1
	v_cndmask_b32_e32 v0, 23, v2, vcc
	v_cmp_lt_i32_e32 vcc, s16, v1
	s_nop 1
	v_cndmask_b32_e32 v2, 24, v0, vcc
	v_mov_b32_e32 v0, v152
	v_mov_b32_e32 v1, v153
	v_readlane_b32 s17, v254, 63
	s_waitcnt lgkmcnt(0)
	v_cmp_lt_i32_e32 vcc, s16, v0
	s_nop 1
	v_cndmask_b32_e32 v0, 25, v2, vcc
	v_cmp_lt_i32_e32 vcc, s16, v1
	s_nop 1
	v_cndmask_b32_e32 v2, 26, v0, vcc
	v_mov_b32_e32 v0, v154
	v_mov_b32_e32 v1, v155
	v_readlane_b32 s17, v255, 1
	s_waitcnt lgkmcnt(0)
	v_cmp_lt_i32_e32 vcc, s16, v0
	s_nop 1
	v_cndmask_b32_e32 v0, 27, v2, vcc
	v_cmp_lt_i32_e32 vcc, s16, v1
	s_nop 1
	v_cndmask_b32_e32 v2, 28, v0, vcc
	v_mov_b32_e32 v0, v156
	v_mov_b32_e32 v1, v157
	v_readlane_b32 s17, v255, 2
	s_waitcnt lgkmcnt(0)
	v_cmp_lt_i32_e32 vcc, s16, v0
	s_nop 1
	v_cndmask_b32_e32 v0, 29, v2, vcc
	v_cmp_lt_i32_e32 vcc, s16, v1
	v_mov_b32_e32 v1, s17
	ds_read_b32 v1, v1
	v_cndmask_b32_e32 v0, 30, v0, vcc
	s_waitcnt lgkmcnt(0)
	v_cmp_lt_i32_e32 vcc, s16, v1
	s_nop 1
	v_cndmask_b32_e32 v0, 31, v0, vcc
	v_lshlrev_b32_e32 v1, 2, v0
	v_add_u32_e32 v1, 0, v1
	v_add_u32_e32 v2, 0x24000, v1
	ds_read_b32 v2, v2
	v_add_u32_e32 v1, 0x24100, v1
	ds_read_b32 v1, v1
	s_waitcnt lgkmcnt(1)
	v_readfirstlane_b32 s17, v2
	s_addk_i32 s17, 0xff
	s_ashr_i32 s17, s17, 8
	s_abs_i32 s21, s17
	s_waitcnt lgkmcnt(0)
	v_readfirstlane_b32 s19, v1
	v_cvt_f32_u32_e32 v1, s21
	s_sub_i32 s24, 0, s21
	s_sub_i32 s16, s16, s19
	s_abs_i32 s20, s16
	v_rcp_iflag_f32_e32 v1, v1
	s_xor_b32 s19, s16, s17
	s_ashr_i32 s19, s19, 31
	v_mul_f32_e32 v1, 0x4f7ffffe, v1
	v_cvt_u32_f32_e32 v1, v1
	s_nop 0
	v_readfirstlane_b32 s25, v1
	s_mul_i32 s24, s24, s25
	s_mul_hi_u32 s24, s25, s24
	s_add_i32 s25, s25, s24
	s_mul_hi_u32 s24, s20, s25
	s_mul_i32 s25, s24, s21
	s_sub_i32 s20, s20, s25
	s_add_i32 s25, s24, 1
	s_sub_i32 s26, s20, s21
	s_cmp_ge_u32 s20, s21
	s_cselect_b32 s24, s25, s24
	s_cselect_b32 s20, s26, s20
	s_add_i32 s25, s24, 1
	s_cmp_ge_u32 s20, s21
	s_cselect_b32 s20, s25, s24
	s_xor_b32 s20, s20, s19
	s_sub_i32 s19, s20, s19
	s_mul_i32 s17, s19, s17
	s_sub_i32 s20, s16, s17
	v_lshl_add_u32 v1, s20, 8, v206
	v_cmp_lt_i32_e32 vcc, v1, v2
	s_and_saveexec_b64 s[16:17], vcc
	s_cbranch_execz .LBB0_1112
	v_lshl_add_u32 v2, v0, 13, v1
	v_ashrrev_i32_e32 v3, 31, v2
	v_lshl_add_u64 v[2:3], v[2:3], 2, s[14:15]
	global_load_dword v208, v[2:3], off

.LBB0_1117:
	s_and_b64 vcc, exec, s[4:5]
	s_cbranch_vccnz .LBB0_1127
	v_readlane_b32 s6, v255, 3
	s_nop 1
	v_mov_b32_e32 v0, s6
	ds_read_b32 v0, v0
	s_lshl_b32 s6, s22, 2
	s_add_i32 s16, s23, s6
	s_waitcnt lgkmcnt(0)
	v_cmp_ge_i32_e32 vcc, s16, v0
	s_cbranch_vccnz .LBB0_1127
	s_movk_i32 s6, 0x100
	v_cmp_gt_i32_e32 vcc, s6, v206
	s_and_saveexec_b64 s[6:7], vcc
	s_cbranch_execz .LBB0_1126
	v_readlane_b32 s17, v255, 4
	v_mov_b32_e32 v208, -1
	s_nop 0
	v_readlane_b32 s100, v255, 4
	s_nop 1
	v_mov_b32_e32 v214, s100
	ds_read2_b32 v[128:129], v214 offset1:1
	v_readlane_b32 s100, v254, 45
	s_nop 1
	v_mov_b32_e32 v214, s100
	ds_read2_b32 v[130:131], v214 offset1:1
	v_readlane_b32 s100, v254, 47
	s_nop 1
	v_mov_b32_e32 v214, s100
	ds_read2_b32 v[132:133], v214 offset1:1
	v_readlane_b32 s100, v254, 48
	s_nop 1
	v_mov_b32_e32 v214, s100
	ds_read2_b32 v[134:135], v214 offset1:1
	v_readlane_b32 s100, v254, 50
	s_nop 1
	v_mov_b32_e32 v214, s100
	ds_read2_b32 v[136:137], v214 offset1:1
	v_readlane_b32 s100, v254, 51
	s_nop 1
	v_mov_b32_e32 v214, s100
	ds_read2_b32 v[138:139], v214 offset1:1
	v_readlane_b32 s100, v254, 53
	s_nop 1
	v_mov_b32_e32 v214, s100
	ds_read2_b32 v[140:141], v214 offset1:1
	v_readlane_b32 s100, v254, 54
	s_nop 1
	v_mov_b32_e32 v214, s100
	ds_read2_b32 v[142:143], v214 offset1:1
	s_waitcnt lgkmcnt(0)
	v_readlane_b32 s100, v254, 56
	s_nop 1
	v_mov_b32_e32 v214, s100
	ds_read2_b32 v[144:145], v214 offset1:1
	v_readlane_b32 s100, v254, 57
	s_nop 1
	v_mov_b32_e32 v214, s100
	ds_read2_b32 v[146:147], v214 offset1:1
	v_readlane_b32 s100, v254, 59
	s_nop 1
	v_mov_b32_e32 v214, s100
	ds_read2_b32 v[148:149], v214 offset1:1
	v_readlane_b32 s100, v254, 60
	s_nop 1
	v_mov_b32_e32 v214, s100
	ds_read2_b32 v[150:151], v214 offset1:1
	v_readlane_b32 s100, v254, 62
	s_nop 1
	v_mov_b32_e32 v214, s100
	ds_read2_b32 v[152:153], v214 offset1:1
	v_readlane_b32 s100, v254, 63
	s_nop 1
	v_mov_b32_e32 v214, s100
	ds_read2_b32 v[154:155], v214 offset1:1
	v_readlane_b32 s100, v255, 1
	s_nop 1
	v_mov_b32_e32 v214, s100
	ds_read2_b32 v[156:157], v214 offset1:1
	s_waitcnt lgkmcnt(0)
	v_mov_b32_e32 v0, v128
	v_mov_b32_e32 v1, v129
	v_readlane_b32 s17, v254, 45
	s_waitcnt lgkmcnt(0)
	v_cmp_ge_i32_e32 vcc, s16, v0
	s_nop 1
	v_cndmask_b32_e64 v0, 0, 1, vcc
	v_cmp_lt_i32_e32 vcc, s16, v1
	s_nop 1
	v_cndmask_b32_e32 v2, 2, v0, vcc
	v_mov_b32_e32 v0, v130
	v_mov_b32_e32 v1, v131
	v_readlane_b32 s17, v254, 47
	s_waitcnt lgkmcnt(0)
	v_cmp_lt_i32_e32 vcc, s16, v0
	s_nop 1
	v_cndmask_b32_e32 v0, 3, v2, vcc
	v_cmp_lt_i32_e32 vcc, s16, v1
	s_nop 1
	v_cndmask_b32_e32 v2, 4, v0, vcc
	v_mov_b32_e32 v0, v132
	v_mov_b32_e32 v1, v133
	v_readlane_b32 s17, v254, 48
	s_waitcnt lgkmcnt(0)
	v_cmp_lt_i32_e32 vcc, s16, v0
	s_nop 1
	v_cndmask_b32_e32 v0, 5, v2, vcc
	v_cmp_lt_i32_e32 vcc, s16, v1
	s_nop 1
	v_cndmask_b32_e32 v2, 6, v0, vcc
	v_mov_b32_e32 v0, v134
	v_mov_b32_e32 v1, v135
	v_readlane_b32 s17, v254, 50
	s_waitcnt lgkmcnt(0)
	v_cmp_lt_i32_e32 vcc, s16, v0
	s_nop 1
	v_cndmask_b32_e32 v0, 7, v2, vcc
	v_cmp_lt_i32_e32 vcc, s16, v1
	s_nop 1
	v_cndmask_b32_e32 v2, 8, v0, vcc
	v_mov_b32_e32 v0, v136
	v_mov_b32_e32 v1, v137
	v_readlane_b32 s17, v254, 51
	s_waitcnt lgkmcnt(0)
	v_cmp_lt_i32_e32 vcc, s16, v0
	s_nop 1
	v_cndmask_b32_e32 v0, 9, v2, vcc
	v_cmp_lt_i32_e32 vcc, s16, v1
	s_nop 1
	v_cndmask_b32_e32 v2, 10, v0, vcc
	v_mov_b32_e32 v0, v138
	v_mov_b32_e32 v1, v139
	v_readlane_b32 s17, v254, 53
	s_waitcnt lgkmcnt(0)
	v_cmp_lt_i32_e32 vcc, s16, v0
	s_nop 1
	v_cndmask_b32_e32 v0, 11, v2, vcc
	v_cmp_lt_i32_e32 vcc, s16, v1
	s_nop 1
	v_cndmask_b32_e32 v2, 12, v0, vcc
	v_mov_b32_e32 v0, v140
	v_mov_b32_e32 v1, v141
	v_readlane_b32 s17, v254, 54
	s_waitcnt lgkmcnt(0)
	v_cmp_lt_i32_e32 vcc, s16, v0
	s_nop 1
	v_cndmask_b32_e32 v0, 13, v2, vcc
	v_cmp_lt_i32_e32 vcc, s16, v1
	s_nop 1
	v_cndmask_b32_e32 v2, 14, v0, vcc
	v_mov_b32_e32 v0, v142
	v_mov_b32_e32 v1, v143
	v_readlane_b32 s17, v254, 56
	s_waitcnt lgkmcnt(0)
	v_cmp_lt_i32_e32 vcc, s16, v0
	s_nop 1
	v_cndmask_b32_e32 v0, 15, v2, vcc
	v_cmp_lt_i32_e32 vcc, s16, v1
	s_nop 1
	v_cndmask_b32_e32 v2, 16, v0, vcc
	v_mov_b32_e32 v0, v144
	v_mov_b32_e32 v1, v145
	v_readlane_b32 s17, v254, 57
	s_waitcnt lgkmcnt(0)
	v_cmp_lt_i32_e32 vcc, s16, v0
	s_nop 1
	v_cndmask_b32_e32 v0, 17, v2, vcc
	v_cmp_lt_i32_e32 vcc, s16, v1
	s_nop 1
	v_cndmask_b32_e32 v2, 18, v0, vcc
	v_mov_b32_e32 v0, v146
	v_mov_b32_e32 v1, v147
	v_readlane_b32 s17, v254, 59
	s_waitcnt lgkmcnt(0)
	v_cmp_lt_i32_e32 vcc, s16, v0
	s_nop 1
	v_cndmask_b32_e32 v0, 19, v2, vcc
	v_cmp_lt_i32_e32 vcc, s16, v1
	s_nop 1
	v_cndmask_b32_e32 v2, 20, v0, vcc
	v_mov_b32_e32 v0, v148
	v_mov_b32_e32 v1, v149
	v_readlane_b32 s17, v254, 60
	s_waitcnt lgkmcnt(0)
	v_cmp_lt_i32_e32 vcc, s16, v0
	s_nop 1
	v_cndmask_b32_e32 v0, 21, v2, vcc
	v_cmp_lt_i32_e32 vcc, s16, v1
	s_nop 1
	v_cndmask_b32_e32 v2, 22, v0, vcc
	v_mov_b32_e32 v0, v150
	v_mov_b32_e32 v1, v151
	v_readlane_b32 s17, v254, 62
	s_waitcnt lgkmcnt(0)
	v_cmp_lt_i32_e32 vcc, s16, v0
	s_nop 1
	v_cndmask_b32_e32 v0, 23, v2, vcc
	v_cmp_lt_i32_e32 vcc, s16, v1
	s_nop 1
	v_cndmask_b32_e32 v2, 24, v0, vcc
	v_mov_b32_e32 v0, v152
	v_mov_b32_e32 v1, v153
	v_readlane_b32 s17, v254, 63
	s_waitcnt lgkmcnt(0)
	v_cmp_lt_i32_e32 vcc, s16, v0
	s_nop 1
	v_cndmask_b32_e32 v0, 25, v2, vcc
	v_cmp_lt_i32_e32 vcc, s16, v1
	s_nop 1
	v_cndmask_b32_e32 v2, 26, v0, vcc
	v_mov_b32_e32 v0, v154
	v_mov_b32_e32 v1, v155
	v_readlane_b32 s17, v255, 1
	s_waitcnt lgkmcnt(0)
	v_cmp_lt_i32_e32 vcc, s16, v0
	s_nop 1
	v_cndmask_b32_e32 v0, 27, v2, vcc
	v_cmp_lt_i32_e32 vcc, s16, v1
	s_nop 1
	v_cndmask_b32_e32 v2, 28, v0, vcc
	v_mov_b32_e32 v0, v156
	v_mov_b32_e32 v1, v157
	v_readlane_b32 s17, v255, 2
	s_waitcnt lgkmcnt(0)
	v_cmp_lt_i32_e32 vcc, s16, v0
	s_nop 1
	v_cndmask_b32_e32 v0, 29, v2, vcc
	v_cmp_lt_i32_e32 vcc, s16, v1
	v_mov_b32_e32 v1, s17
	ds_read_b32 v1, v1
	v_cndmask_b32_e32 v0, 30, v0, vcc
	s_waitcnt lgkmcnt(0)
	v_cmp_lt_i32_e32 vcc, s16, v1
	s_nop 1
	v_cndmask_b32_e32 v0, 31, v0, vcc
	v_lshlrev_b32_e32 v1, 2, v0
	v_add_u32_e32 v1, 0, v1
	v_add_u32_e32 v2, 0x24000, v1
	ds_read_b32 v2, v2
	v_add_u32_e32 v1, 0x24100, v1
	ds_read_b32 v1, v1
	s_waitcnt lgkmcnt(1)
	v_readfirstlane_b32 s17, v2
	s_addk_i32 s17, 0xff
	s_ashr_i32 s17, s17, 8
	s_abs_i32 s21, s17
	s_waitcnt lgkmcnt(0)
	v_readfirstlane_b32 s19, v1
	v_cvt_f32_u32_e32 v1, s21
	s_sub_i32 s24, 0, s21
	s_sub_i32 s16, s16, s19
	s_abs_i32 s20, s16
	v_rcp_iflag_f32_e32 v1, v1
	s_xor_b32 s19, s16, s17
	s_ashr_i32 s19, s19, 31
	v_mul_f32_e32 v1, 0x4f7ffffe, v1
	v_cvt_u32_f32_e32 v1, v1
	s_nop 0
	v_readfirstlane_b32 s25, v1
	s_mul_i32 s24, s24, s25
	s_mul_hi_u32 s24, s25, s24
	s_add_i32 s25, s25, s24
	s_mul_hi_u32 s24, s20, s25
	s_mul_i32 s25, s24, s21
	s_sub_i32 s20, s20, s25
	s_add_i32 s25, s24, 1
	s_sub_i32 s26, s20, s21
	s_cmp_ge_u32 s20, s21
	s_cselect_b32 s24, s25, s24
	s_cselect_b32 s20, s26, s20
	s_add_i32 s25, s24, 1
	s_cmp_ge_u32 s20, s21
	s_cselect_b32 s20, s25, s24
	s_xor_b32 s20, s20, s19
	s_sub_i32 s19, s20, s19
	s_mul_i32 s17, s19, s17
	s_sub_i32 s20, s16, s17
	v_lshl_add_u32 v1, s20, 8, v206
	v_cmp_lt_i32_e32 vcc, v1, v2
	s_and_saveexec_b64 s[16:17], vcc
	s_cbranch_execz .LBB0_1122
	v_lshl_add_u32 v2, v0, 13, v1
	v_ashrrev_i32_e32 v3, 31, v2
	v_lshl_add_u64 v[2:3], v[2:3], 2, s[14:15]
	global_load_dword v208, v[2:3], off

.LBB0_1127:
	s_and_b64 vcc, exec, s[4:5]
	s_mov_b64 s[4:5], -1
	s_cbranch_vccnz .LBB0_1138
	v_readlane_b32 s4, v255, 3
	s_nop 1
	v_mov_b32_e32 v0, s4
	ds_read_b32 v0, v0
	s_mul_i32 s4, s22, 5
	s_add_i32 s6, s23, s4
	s_waitcnt lgkmcnt(0)
	v_cmp_lt_i32_e32 vcc, s6, v0
	v_cmp_ge_i32_e64 s[4:5], s6, v0
	s_cbranch_vccz .LBB0_1138
	v_readlane_b32 s7, v255, 4
	s_nop 1
	v_readlane_b32 s100, v255, 4
	s_nop 1
	v_mov_b32_e32 v214, s100
	ds_read2_b32 v[128:129], v214 offset1:1
	v_readlane_b32 s100, v254, 45
	s_nop 1
	v_mov_b32_e32 v214, s100
	ds_read2_b32 v[130:131], v214 offset1:1
	v_readlane_b32 s100, v254, 47
	s_nop 1
	v_mov_b32_e32 v214, s100
	ds_read2_b32 v[132:133], v214 offset1:1
	v_readlane_b32 s100, v254, 48
	s_nop 1
	v_mov_b32_e32 v214, s100
	ds_read2_b32 v[134:135], v214 offset1:1
	v_readlane_b32 s100, v254, 50
	s_nop 1
	v_mov_b32_e32 v214, s100
	ds_read2_b32 v[136:137], v214 offset1:1
	v_readlane_b32 s100, v254, 51
	s_nop 1
	v_mov_b32_e32 v214, s100
	ds_read2_b32 v[138:139], v214 offset1:1
	v_readlane_b32 s100, v254, 53
	s_nop 1
	v_mov_b32_e32 v214, s100
	ds_read2_b32 v[140:141], v214 offset1:1
	v_readlane_b32 s100, v254, 54
	s_nop 1
	v_mov_b32_e32 v214, s100
	ds_read2_b32 v[142:143], v214 offset1:1
	s_waitcnt lgkmcnt(0)
	v_readlane_b32 s100, v254, 56
	s_nop 1
	v_mov_b32_e32 v214, s100
	ds_read2_b32 v[144:145], v214 offset1:1
	v_readlane_b32 s100, v254, 57
	s_nop 1
	v_mov_b32_e32 v214, s100
	ds_read2_b32 v[146:147], v214 offset1:1
	v_readlane_b32 s100, v254, 59
	s_nop 1
	v_mov_b32_e32 v214, s100
	ds_read2_b32 v[148:149], v214 offset1:1
	v_readlane_b32 s100, v254, 60
	s_nop 1
	v_mov_b32_e32 v214, s100
	ds_read2_b32 v[150:151], v214 offset1:1
	v_readlane_b32 s100, v254, 62
	s_nop 1
	v_mov_b32_e32 v214, s100
	ds_read2_b32 v[152:153], v214 offset1:1
	v_readlane_b32 s100, v254, 63
	s_nop 1
	v_mov_b32_e32 v214, s100
	ds_read2_b32 v[154:155], v214 offset1:1
	v_readlane_b32 s100, v255, 1
	s_nop 1
	v_mov_b32_e32 v214, s100
	ds_read2_b32 v[156:157], v214 offset1:1
	s_waitcnt lgkmcnt(0)
	v_mov_b32_e32 v0, v128
	v_mov_b32_e32 v1, v129
	v_readlane_b32 s7, v254, 45
	s_waitcnt lgkmcnt(0)
	v_cmp_ge_i32_e32 vcc, s6, v0
	s_nop 1
	v_cndmask_b32_e64 v0, 0, 1, vcc
	v_cmp_lt_i32_e32 vcc, s6, v1
	s_nop 1
	v_cndmask_b32_e32 v2, 2, v0, vcc
	v_mov_b32_e32 v0, v130
	v_mov_b32_e32 v1, v131
	v_readlane_b32 s7, v254, 47
	s_waitcnt lgkmcnt(0)
	v_cmp_lt_i32_e32 vcc, s6, v0
	s_nop 1
	v_cndmask_b32_e32 v0, 3, v2, vcc
	v_cmp_lt_i32_e32 vcc, s6, v1
	s_nop 1
	v_cndmask_b32_e32 v2, 4, v0, vcc
	v_mov_b32_e32 v0, v132
	v_mov_b32_e32 v1, v133
	v_readlane_b32 s7, v254, 48
	s_waitcnt lgkmcnt(0)
	v_cmp_lt_i32_e32 vcc, s6, v0
	s_nop 1
	v_cndmask_b32_e32 v0, 5, v2, vcc
	v_cmp_lt_i32_e32 vcc, s6, v1
	s_nop 1
	v_cndmask_b32_e32 v2, 6, v0, vcc
	v_mov_b32_e32 v0, v134
	v_mov_b32_e32 v1, v135
	v_readlane_b32 s7, v254, 50
	s_waitcnt lgkmcnt(0)
	v_cmp_lt_i32_e32 vcc, s6, v0
	s_nop 1
	v_cndmask_b32_e32 v0, 7, v2, vcc
	v_cmp_lt_i32_e32 vcc, s6, v1
	s_nop 1
	v_cndmask_b32_e32 v2, 8, v0, vcc
	v_mov_b32_e32 v0, v136
	v_mov_b32_e32 v1, v137
	v_readlane_b32 s7, v254, 51
	s_waitcnt lgkmcnt(0)
	v_cmp_lt_i32_e32 vcc, s6, v0
	s_nop 1
	v_cndmask_b32_e32 v0, 9, v2, vcc
	v_cmp_lt_i32_e32 vcc, s6, v1
	s_nop 1
	v_cndmask_b32_e32 v2, 10, v0, vcc
	v_mov_b32_e32 v0, v138
	v_mov_b32_e32 v1, v139
	v_readlane_b32 s7, v254, 53
	s_waitcnt lgkmcnt(0)
	v_cmp_lt_i32_e32 vcc, s6, v0
	s_nop 1
	v_cndmask_b32_e32 v0, 11, v2, vcc
	v_cmp_lt_i32_e32 vcc, s6, v1
	s_nop 1
	v_cndmask_b32_e32 v2, 12, v0, vcc
	v_mov_b32_e32 v0, v140
	v_mov_b32_e32 v1, v141
	v_readlane_b32 s7, v254, 54
	s_waitcnt lgkmcnt(0)
	v_cmp_lt_i32_e32 vcc, s6, v0
	s_nop 1
	v_cndmask_b32_e32 v0, 13, v2, vcc
	v_cmp_lt_i32_e32 vcc, s6, v1
	s_nop 1
	v_cndmask_b32_e32 v2, 14, v0, vcc
	v_mov_b32_e32 v0, v142
	v_mov_b32_e32 v1, v143
	v_readlane_b32 s7, v254, 56
	s_waitcnt lgkmcnt(0)
	v_cmp_lt_i32_e32 vcc, s6, v0
	s_nop 1
	v_cndmask_b32_e32 v0, 15, v2, vcc
	v_cmp_lt_i32_e32 vcc, s6, v1
	s_nop 1
	v_cndmask_b32_e32 v2, 16, v0, vcc
	v_mov_b32_e32 v0, v144
	v_mov_b32_e32 v1, v145
	v_readlane_b32 s7, v254, 57
	s_waitcnt lgkmcnt(0)
	v_cmp_lt_i32_e32 vcc, s6, v0
	s_nop 1
	v_cndmask_b32_e32 v0, 17, v2, vcc
	v_cmp_lt_i32_e32 vcc, s6, v1
	s_nop 1
	v_cndmask_b32_e32 v2, 18, v0, vcc
	v_mov_b32_e32 v0, v146
	v_mov_b32_e32 v1, v147
	v_readlane_b32 s7, v254, 59
	s_waitcnt lgkmcnt(0)
	v_cmp_lt_i32_e32 vcc, s6, v0
	s_nop 1
	v_cndmask_b32_e32 v0, 19, v2, vcc
	v_cmp_lt_i32_e32 vcc, s6, v1
	s_nop 1
	v_cndmask_b32_e32 v2, 20, v0, vcc
	v_mov_b32_e32 v0, v148
	v_mov_b32_e32 v1, v149
	v_readlane_b32 s7, v254, 60
	s_waitcnt lgkmcnt(0)
	v_cmp_lt_i32_e32 vcc, s6, v0
	s_nop 1
	v_cndmask_b32_e32 v0, 21, v2, vcc
	v_cmp_lt_i32_e32 vcc, s6, v1
	s_nop 1
	v_cndmask_b32_e32 v2, 22, v0, vcc
	v_mov_b32_e32 v0, v150
	v_mov_b32_e32 v1, v151
	v_readlane_b32 s7, v254, 62
	s_waitcnt lgkmcnt(0)
	v_cmp_lt_i32_e32 vcc, s6, v0
	s_nop 1
	v_cndmask_b32_e32 v0, 23, v2, vcc
	v_cmp_lt_i32_e32 vcc, s6, v1
	s_nop 1
	v_cndmask_b32_e32 v2, 24, v0, vcc
	v_mov_b32_e32 v0, v152
	v_mov_b32_e32 v1, v153
	v_readlane_b32 s7, v254, 63
	s_waitcnt lgkmcnt(0)
	v_cmp_lt_i32_e32 vcc, s6, v0
	s_nop 1
	v_cndmask_b32_e32 v0, 25, v2, vcc
	v_cmp_lt_i32_e32 vcc, s6, v1
	s_nop 1
	v_cndmask_b32_e32 v2, 26, v0, vcc
	v_mov_b32_e32 v0, v154
	v_mov_b32_e32 v1, v155
	v_readlane_b32 s7, v255, 1
	s_waitcnt lgkmcnt(0)
	v_cmp_lt_i32_e32 vcc, s6, v0
	s_nop 1
	v_cndmask_b32_e32 v0, 27, v2, vcc
	v_cmp_lt_i32_e32 vcc, s6, v1
	s_nop 1
	v_cndmask_b32_e32 v2, 28, v0, vcc
	v_mov_b32_e32 v0, v156
	v_mov_b32_e32 v1, v157
	v_readlane_b32 s7, v255, 2
	s_waitcnt lgkmcnt(0)
	v_cmp_lt_i32_e32 vcc, s6, v0
	s_nop 1
	v_cndmask_b32_e32 v0, 29, v2, vcc
	v_cmp_lt_i32_e32 vcc, s6, v1
	v_mov_b32_e32 v1, s7
	ds_read_b32 v1, v1
	v_cndmask_b32_e32 v0, 30, v0, vcc
	s_waitcnt lgkmcnt(0)
	v_cmp_lt_i32_e32 vcc, s6, v1
	s_nop 1
	v_cndmask_b32_e32 v0, 31, v0, vcc
	v_lshlrev_b32_e32 v1, 2, v0
	v_add_u32_e32 v2, 0, v1
	v_add_u32_e32 v1, 0x24000, v2
	ds_read_b32 v1, v1
	v_add_u32_e32 v2, 0x24100, v2
	ds_read_b32 v2, v2
	s_waitcnt lgkmcnt(1)
	v_readfirstlane_b32 s7, v1
	s_addk_i32 s7, 0xff
	s_ashr_i32 s7, s7, 8
	s_abs_i32 s19, s7
	s_waitcnt lgkmcnt(0)
	v_readfirstlane_b32 s16, v2
	v_cvt_f32_u32_e32 v2, s19
	s_sub_i32 s20, 0, s19
	s_sub_i32 s6, s6, s16
	s_abs_i32 s17, s6
	v_rcp_iflag_f32_e32 v2, v2
	s_xor_b32 s16, s6, s7
	s_ashr_i32 s16, s16, 31
	v_mul_f32_e32 v2, 0x4f7ffffe, v2
	v_cvt_u32_f32_e32 v2, v2
	s_nop 0
	v_readfirstlane_b32 s21, v2
	s_mul_i32 s20, s20, s21
	s_mul_hi_u32 s20, s21, s20
	s_add_i32 s21, s21, s20
	s_mul_hi_u32 s20, s17, s21
	s_mul_i32 s21, s20, s19
	s_sub_i32 s17, s17, s21
	s_add_i32 s21, s20, 1
	s_sub_i32 s24, s17, s19
	s_cmp_ge_u32 s17, s19
	s_cselect_b32 s20, s21, s20
	s_cselect_b32 s17, s24, s17
	s_add_i32 s21, s20, 1
	s_cmp_ge_u32 s17, s19
	s_cselect_b32 s17, s21, s20
	s_xor_b32 s17, s17, s16
	s_sub_i32 s19, s17, s16
	s_mul_i32 s7, s19, s7
	s_sub_i32 s20, s6, s7
	s_movk_i32 s6, 0x100
	v_cmp_gt_i32_e32 vcc, s6, v206
	s_and_saveexec_b64 s[6:7], vcc
	s_cbranch_execz .LBB0_1135
	v_lshl_add_u32 v2, s20, 8, v206
	v_cmp_lt_i32_e32 vcc, v2, v1
	v_mov_b32_e32 v208, -1
	s_and_saveexec_b64 s[16:17], vcc
	s_cbranch_execz .LBB0_1132
	v_lshl_add_u32 v2, v0, 13, v2
	v_ashrrev_i32_e32 v3, 31, v2
	v_lshl_add_u64 v[2:3], v[2:3], 2, s[14:15]
	global_load_dword v208, v[2:3], off

.LBB0_1156:
	s_add_u32 s4, s25, s43
	s_addc_u32 s5, s26, 0
	v_lshlrev_b32_e32 v208, 4, v207
	v_lshl_add_u64 v[128:129], s[4:5], 0, v[208:209]
	s_add_i32 s4, s42, 0x24198
	v_mov_b32_e32 v130, s4
	v_lshl_or_b32 v131, s40, 7, v220
	ds_read_b32 v132, v130
	v_lshl_add_u32 v130, s27, 8, v131
	v_lshl_add_u32 v131, v131, 2, s31
	ds_read_b32 v208, v131
	s_waitcnt lgkmcnt(0)
	v_lshlrev_b32_e32 v132, 7, v132
	v_ashrrev_i32_e32 v133, 31, v132
	v_lshl_add_u64 v[128:129], v[132:133], 1, v[128:129]
	v_cmp_lt_i32_e32 vcc, -1, v208
	s_and_saveexec_b64 s[4:5], vcc
	s_cbranch_execz .LBB0_1158
	v_lshl_add_u32 v131, v130, 2, 0
	v_add_u32_e32 v131, 0x25a00, v131
	ds_read_b32 v132, v131
	v_mul_f32_e32 v131, 0xbfb8aa3b, v124
	v_exp_f32_e32 v131, v131
	v_mul_f32_e32 v133, 0xbfb8aa3b, v120
	v_exp_f32_e32 v133, v133
	v_mov_b32_e32 v138, v124
	v_add_f32_e32 v131, 1.0, v131
	v_rcp_f32_e32 v136, v131
	v_add_f32_e32 v131, 1.0, v133
	v_rcp_f32_e32 v137, v131
	v_mov_b32_e32 v139, v120
	v_mov_b32_e32 v120, v125
	v_lshlrev_b64 v[134:135], 10, v[208:209]
	v_pk_mul_f32 v[136:137], v[138:139], v[136:137]
	v_mov_b32_e32 v139, v112
	v_mul_f32_e32 v112, 0xbfb8aa3b, v125
	v_mov_b32_e32 v138, v116
	v_exp_f32_e32 v112, v112
	v_mul_f32_e32 v116, 0xbfb8aa3b, v121
	v_exp_f32_e32 v116, v116
	v_pk_mul_f32 v[136:137], v[138:139], v[136:137]
	v_add_f32_e32 v112, 1.0, v112
	v_rcp_f32_e32 v138, v112
	v_add_f32_e32 v112, 1.0, v116
	v_rcp_f32_e32 v139, v112
	v_mov_b32_e32 v112, v117
	v_mul_f32_e32 v117, 0xbfb8aa3b, v126
	v_exp_f32_e32 v117, v117
	v_pk_mul_f32 v[120:121], v[120:121], v[138:139]
	s_waitcnt lgkmcnt(0)
	v_pk_mul_f32 v[136:137], v[136:137], v[132:133] op_sel_hi:[1,0]
	v_pk_mul_f32 v[112:113], v[112:113], v[120:121]
	v_mul_f32_e32 v120, 0xbfb8aa3b, v122
	v_exp_f32_e32 v121, v120
	v_add_f32_e32 v117, 1.0, v117
	v_rcp_f32_e32 v120, v117
	v_pk_mul_f32 v[112:113], v[112:113], v[132:133] op_sel_hi:[1,0]
	v_add_f32_e32 v117, 1.0, v121
	v_rcp_f32_e32 v121, v117
	v_cvt_pk_bf16_f32 v117, v112, v113
	v_mov_b32_e32 v112, v126
	v_mov_b32_e32 v113, v122
	v_pk_mul_f32 v[112:113], v[112:113], v[120:121]
	v_mov_b32_e32 v121, v114
	v_mul_f32_e32 v114, 0xbfb8aa3b, v127
	v_mov_b32_e32 v120, v118
	v_exp_f32_e32 v114, v114
	v_mul_f32_e32 v118, 0xbfb8aa3b, v123
	v_exp_f32_e32 v118, v118
	v_pk_mul_f32 v[112:113], v[120:121], v[112:113]
	v_add_f32_e32 v114, 1.0, v114
	v_rcp_f32_e32 v120, v114
	v_add_f32_e32 v114, 1.0, v118
	v_rcp_f32_e32 v121, v114
	v_pk_mul_f32 v[112:113], v[112:113], v[132:133] op_sel_hi:[1,0]
	v_mov_b32_e32 v122, v127
	v_cvt_pk_bf16_f32 v118, v112, v113
	v_pk_mul_f32 v[112:113], v[122:123], v[120:121]
	v_mov_b32_e32 v114, v119
	v_pk_mul_f32 v[112:113], v[114:115], v[112:113]
	v_lshl_add_u64 v[134:135], v[128:129], 0, v[134:135]
	v_pk_mul_f32 v[112:113], v[112:113], v[132:133] op_sel_hi:[1,0]
	v_cvt_pk_bf16_f32 v116, v136, v137
	v_cvt_pk_bf16_f32 v119, v112, v113
	global_store_dwordx4 v[134:135], v[116:119], off sc0 sc1
.LBB0_1158:
	s_or_b64 exec, exec, s[4:5]
	v_or_b32_e32 v112, 16, v130
	v_lshl_add_u32 v112, v112, 2, 0
	v_add_u32_e32 v113, 0x24200, v112
	ds_read_b32 v208, v113
	s_waitcnt lgkmcnt(0)
	v_cmp_lt_i32_e32 vcc, -1, v208
	s_and_saveexec_b64 s[4:5], vcc
	s_cbranch_execz .LBB0_1160
	v_mul_f32_e32 v113, 0xbfb8aa3b, v96
	v_exp_f32_e32 v113, v113
	v_mul_f32_e32 v114, 0xbfb8aa3b, v100
	v_exp_f32_e32 v117, v114
	v_mov_b32_e32 v118, v96
	v_add_f32_e32 v113, 1.0, v113
	v_rcp_f32_e32 v116, v113
	v_add_f32_e32 v113, 1.0, v117
	v_mul_f32_e32 v96, 0xbfb8aa3b, v97
	v_rcp_f32_e32 v117, v113
	v_mov_b32_e32 v119, v100
	v_exp_f32_e32 v96, v96
	v_mul_f32_e32 v100, 0xbfb8aa3b, v101
	v_exp_f32_e32 v100, v100
	v_pk_mul_f32 v[116:117], v[118:119], v[116:117]
	v_mov_b32_e32 v118, v104
	v_mov_b32_e32 v119, v108
	v_add_f32_e32 v96, 1.0, v96
	v_pk_mul_f32 v[116:117], v[118:119], v[116:117]
	v_rcp_f32_e32 v118, v96
	v_add_f32_e32 v96, 1.0, v100
	v_add_u32_e32 v112, 0x25a00, v112
	v_rcp_f32_e32 v119, v96
	v_mov_b32_e32 v100, v97
	v_mul_f32_e32 v97, 0xbfb8aa3b, v98
	ds_read_b32 v112, v112
	v_exp_f32_e32 v97, v97
	v_mul_f32_e32 v104, 0xbfb8aa3b, v102
	v_mov_b32_e32 v108, v105
	v_exp_f32_e32 v105, v104
	v_pk_mul_f32 v[100:101], v[100:101], v[118:119]
	v_add_f32_e32 v97, 1.0, v97
	v_pk_mul_f32 v[100:101], v[108:109], v[100:101]
	v_rcp_f32_e32 v104, v97
	s_waitcnt lgkmcnt(0)
	v_pk_mul_f32 v[100:101], v[100:101], v[112:113] op_sel_hi:[1,0]
	v_add_f32_e32 v97, 1.0, v105
	v_rcp_f32_e32 v105, v97
	v_cvt_pk_bf16_f32 v97, v100, v101
	v_mov_b32_e32 v100, v98
	v_mul_f32_e32 v98, 0xbfb8aa3b, v99
	v_mov_b32_e32 v101, v102
	v_exp_f32_e32 v98, v98
	v_mul_f32_e32 v102, 0xbfb8aa3b, v103
	v_exp_f32_e32 v102, v102
	v_pk_mul_f32 v[100:101], v[100:101], v[104:105]
	v_mov_b32_e32 v104, v106
	v_mov_b32_e32 v105, v110
	v_add_f32_e32 v98, 1.0, v98
	v_pk_mul_f32 v[100:101], v[104:105], v[100:101]
	v_rcp_f32_e32 v104, v98
	v_add_f32_e32 v98, 1.0, v102
	v_rcp_f32_e32 v105, v98
	v_pk_mul_f32 v[100:101], v[100:101], v[112:113] op_sel_hi:[1,0]
	v_mov_b32_e32 v102, v99
	v_cvt_pk_bf16_f32 v98, v100, v101
	v_pk_mul_f32 v[100:101], v[102:103], v[104:105]
	v_mov_b32_e32 v110, v107
	v_pk_mul_f32 v[100:101], v[110:111], v[100:101]
	v_lshlrev_b64 v[114:115], 10, v[208:209]
	v_pk_mul_f32 v[116:117], v[116:117], v[112:113] op_sel_hi:[1,0]
	v_pk_mul_f32 v[100:101], v[100:101], v[112:113] op_sel_hi:[1,0]
	v_lshl_add_u64 v[114:115], v[128:129], 0, v[114:115]
	v_cvt_pk_bf16_f32 v96, v116, v117
	v_cvt_pk_bf16_f32 v99, v100, v101
	global_store_dwordx4 v[114:115], v[96:99], off sc0 sc1
.LBB0_1160:
	s_or_b64 exec, exec, s[4:5]
	s_nop 0
	v_or_b32_e32 v96, 32, v130
	v_lshl_add_u32 v96, v96, 2, 0
	v_add_u32_e32 v97, 0x24200, v96
	ds_read_b32 v208, v97
	s_waitcnt lgkmcnt(0)
	v_cmp_lt_i32_e32 vcc, -1, v208
	s_and_saveexec_b64 s[4:5], vcc
	s_cbranch_execz .LBB0_1162
	v_mul_f32_e32 v97, 0xbfb8aa3b, v80
	v_exp_f32_e32 v97, v97
	v_mul_f32_e32 v98, 0xbfb8aa3b, v84
	v_exp_f32_e32 v101, v98
	v_mov_b32_e32 v102, v80
	v_add_f32_e32 v97, 1.0, v97
	v_rcp_f32_e32 v100, v97
	v_add_f32_e32 v97, 1.0, v101
	v_mul_f32_e32 v80, 0xbfb8aa3b, v81
	v_rcp_f32_e32 v101, v97
	v_mov_b32_e32 v103, v84
	v_exp_f32_e32 v80, v80
	v_mul_f32_e32 v84, 0xbfb8aa3b, v85
	v_exp_f32_e32 v84, v84
	v_pk_mul_f32 v[100:101], v[102:103], v[100:101]
	v_mov_b32_e32 v102, v88
	v_mov_b32_e32 v103, v92
	v_add_f32_e32 v80, 1.0, v80
	v_pk_mul_f32 v[100:101], v[102:103], v[100:101]
	v_rcp_f32_e32 v102, v80
	v_add_f32_e32 v80, 1.0, v84
	v_add_u32_e32 v96, 0x25a00, v96
	v_rcp_f32_e32 v103, v80
	v_mov_b32_e32 v84, v81
	v_mul_f32_e32 v81, 0xbfb8aa3b, v82
	ds_read_b32 v96, v96
	v_exp_f32_e32 v81, v81
	v_mul_f32_e32 v88, 0xbfb8aa3b, v86
	v_mov_b32_e32 v92, v89
	v_exp_f32_e32 v89, v88
	v_pk_mul_f32 v[84:85], v[84:85], v[102:103]
	v_add_f32_e32 v81, 1.0, v81
	v_pk_mul_f32 v[84:85], v[92:93], v[84:85]
	v_rcp_f32_e32 v88, v81
	s_waitcnt lgkmcnt(0)
	v_pk_mul_f32 v[84:85], v[84:85], v[96:97] op_sel_hi:[1,0]
	v_add_f32_e32 v81, 1.0, v89
	v_rcp_f32_e32 v89, v81
	v_cvt_pk_bf16_f32 v81, v84, v85
	v_mov_b32_e32 v84, v82
	v_mul_f32_e32 v82, 0xbfb8aa3b, v83
	v_mov_b32_e32 v85, v86
	v_exp_f32_e32 v82, v82
	v_mul_f32_e32 v86, 0xbfb8aa3b, v87
	v_exp_f32_e32 v86, v86
	v_pk_mul_f32 v[84:85], v[84:85], v[88:89]
	v_mov_b32_e32 v88, v90
	v_mov_b32_e32 v89, v94
	v_add_f32_e32 v82, 1.0, v82
	v_pk_mul_f32 v[84:85], v[88:89], v[84:85]
	v_rcp_f32_e32 v88, v82
	v_add_f32_e32 v82, 1.0, v86
	v_rcp_f32_e32 v89, v82
	v_pk_mul_f32 v[84:85], v[84:85], v[96:97] op_sel_hi:[1,0]
	v_mov_b32_e32 v86, v83
	v_cvt_pk_bf16_f32 v82, v84, v85
	v_pk_mul_f32 v[84:85], v[86:87], v[88:89]
	v_mov_b32_e32 v94, v91
	v_pk_mul_f32 v[84:85], v[94:95], v[84:85]
	v_lshlrev_b64 v[98:99], 10, v[208:209]
	v_pk_mul_f32 v[100:101], v[100:101], v[96:97] op_sel_hi:[1,0]
	v_pk_mul_f32 v[84:85], v[84:85], v[96:97] op_sel_hi:[1,0]
	v_lshl_add_u64 v[98:99], v[128:129], 0, v[98:99]
	v_cvt_pk_bf16_f32 v80, v100, v101
	v_cvt_pk_bf16_f32 v83, v84, v85
	global_store_dwordx4 v[98:99], v[80:83], off sc0 sc1
.LBB0_1162:
	s_or_b64 exec, exec, s[4:5]
	s_nop 0
	v_or_b32_e32 v80, 48, v130
	v_lshl_add_u32 v80, v80, 2, 0
	v_add_u32_e32 v81, 0x24200, v80
	ds_read_b32 v208, v81
	s_waitcnt lgkmcnt(0)
	v_cmp_lt_i32_e32 vcc, -1, v208
	s_and_saveexec_b64 s[4:5], vcc
	s_cbranch_execz .LBB0_1164
	v_mul_f32_e32 v81, 0xbfb8aa3b, v64
	v_exp_f32_e32 v81, v81
	v_mul_f32_e32 v82, 0xbfb8aa3b, v68
	v_exp_f32_e32 v85, v82
	v_mov_b32_e32 v86, v64
	v_add_f32_e32 v81, 1.0, v81
	v_rcp_f32_e32 v84, v81
	v_add_f32_e32 v81, 1.0, v85
	v_mul_f32_e32 v64, 0xbfb8aa3b, v65
	v_rcp_f32_e32 v85, v81
	v_mov_b32_e32 v87, v68
	v_exp_f32_e32 v64, v64
	v_mul_f32_e32 v68, 0xbfb8aa3b, v69
	v_exp_f32_e32 v68, v68
	v_pk_mul_f32 v[84:85], v[86:87], v[84:85]
	v_mov_b32_e32 v86, v72
	v_mov_b32_e32 v87, v76
	v_add_f32_e32 v64, 1.0, v64
	v_pk_mul_f32 v[84:85], v[86:87], v[84:85]
	v_rcp_f32_e32 v86, v64
	v_add_f32_e32 v64, 1.0, v68
	v_add_u32_e32 v80, 0x25a00, v80
	v_rcp_f32_e32 v87, v64
	v_mov_b32_e32 v68, v65
	v_mul_f32_e32 v65, 0xbfb8aa3b, v66
	ds_read_b32 v80, v80
	v_exp_f32_e32 v65, v65
	v_mul_f32_e32 v72, 0xbfb8aa3b, v70
	v_mov_b32_e32 v76, v73
	v_exp_f32_e32 v73, v72
	v_pk_mul_f32 v[68:69], v[68:69], v[86:87]
	v_add_f32_e32 v65, 1.0, v65
	v_pk_mul_f32 v[68:69], v[76:77], v[68:69]
	v_rcp_f32_e32 v72, v65
	s_waitcnt lgkmcnt(0)
	v_pk_mul_f32 v[68:69], v[68:69], v[80:81] op_sel_hi:[1,0]
	v_add_f32_e32 v65, 1.0, v73
	v_rcp_f32_e32 v73, v65
	v_cvt_pk_bf16_f32 v65, v68, v69
	v_mov_b32_e32 v68, v66
	v_mul_f32_e32 v66, 0xbfb8aa3b, v67
	v_mov_b32_e32 v69, v70
	v_exp_f32_e32 v66, v66
	v_mul_f32_e32 v70, 0xbfb8aa3b, v71
	v_exp_f32_e32 v70, v70
	v_pk_mul_f32 v[68:69], v[68:69], v[72:73]
	v_mov_b32_e32 v72, v74
	v_mov_b32_e32 v73, v78
	v_add_f32_e32 v66, 1.0, v66
	v_pk_mul_f32 v[68:69], v[72:73], v[68:69]
	v_rcp_f32_e32 v72, v66
	v_add_f32_e32 v66, 1.0, v70
	v_rcp_f32_e32 v73, v66
	v_pk_mul_f32 v[68:69], v[68:69], v[80:81] op_sel_hi:[1,0]
	v_mov_b32_e32 v70, v67
	v_cvt_pk_bf16_f32 v66, v68, v69
	v_pk_mul_f32 v[68:69], v[70:71], v[72:73]
	v_mov_b32_e32 v78, v75
	v_pk_mul_f32 v[68:69], v[78:79], v[68:69]
	v_lshlrev_b64 v[82:83], 10, v[208:209]
	v_pk_mul_f32 v[84:85], v[84:85], v[80:81] op_sel_hi:[1,0]
	v_pk_mul_f32 v[68:69], v[68:69], v[80:81] op_sel_hi:[1,0]
	v_lshl_add_u64 v[82:83], v[128:129], 0, v[82:83]
	v_cvt_pk_bf16_f32 v64, v84, v85
	v_cvt_pk_bf16_f32 v67, v68, v69
	global_store_dwordx4 v[82:83], v[64:67], off sc0 sc1
.LBB0_1164:
	s_or_b64 exec, exec, s[4:5]
	s_nop 0
	v_or_b32_e32 v64, 64, v130
	v_lshl_add_u32 v64, v64, 2, 0
	v_add_u32_e32 v65, 0x24200, v64
	ds_read_b32 v208, v65
	s_waitcnt lgkmcnt(0)
	v_cmp_lt_i32_e32 vcc, -1, v208
	s_and_saveexec_b64 s[4:5], vcc
	s_cbranch_execz .LBB0_1166
	v_mul_f32_e32 v65, 0xbfb8aa3b, v48
	v_exp_f32_e32 v65, v65
	v_mul_f32_e32 v66, 0xbfb8aa3b, v52
	v_exp_f32_e32 v69, v66
	v_mov_b32_e32 v70, v48
	v_add_f32_e32 v65, 1.0, v65
	v_rcp_f32_e32 v68, v65
	v_add_f32_e32 v65, 1.0, v69
	v_mul_f32_e32 v48, 0xbfb8aa3b, v49
	v_rcp_f32_e32 v69, v65
	v_mov_b32_e32 v71, v52
	v_exp_f32_e32 v48, v48
	v_mul_f32_e32 v52, 0xbfb8aa3b, v53
	v_exp_f32_e32 v52, v52
	v_pk_mul_f32 v[68:69], v[70:71], v[68:69]
	v_mov_b32_e32 v70, v56
	v_mov_b32_e32 v71, v60
	v_add_f32_e32 v48, 1.0, v48
	v_pk_mul_f32 v[68:69], v[70:71], v[68:69]
	v_rcp_f32_e32 v70, v48
	v_add_f32_e32 v48, 1.0, v52
	v_add_u32_e32 v64, 0x25a00, v64
	v_rcp_f32_e32 v71, v48
	v_mov_b32_e32 v52, v49
	v_mul_f32_e32 v49, 0xbfb8aa3b, v50
	ds_read_b32 v64, v64
	v_exp_f32_e32 v49, v49
	v_mul_f32_e32 v56, 0xbfb8aa3b, v54
	v_mov_b32_e32 v60, v57
	v_exp_f32_e32 v57, v56
	v_pk_mul_f32 v[52:53], v[52:53], v[70:71]
	v_add_f32_e32 v49, 1.0, v49
	v_pk_mul_f32 v[52:53], v[60:61], v[52:53]
	v_rcp_f32_e32 v56, v49
	s_waitcnt lgkmcnt(0)
	v_pk_mul_f32 v[52:53], v[52:53], v[64:65] op_sel_hi:[1,0]
	v_add_f32_e32 v49, 1.0, v57
	v_rcp_f32_e32 v57, v49
	v_cvt_pk_bf16_f32 v49, v52, v53
	v_mov_b32_e32 v52, v50
	v_mul_f32_e32 v50, 0xbfb8aa3b, v51
	v_mov_b32_e32 v53, v54
	v_exp_f32_e32 v50, v50
	v_mul_f32_e32 v54, 0xbfb8aa3b, v55
	v_exp_f32_e32 v54, v54
	v_pk_mul_f32 v[52:53], v[52:53], v[56:57]
	v_mov_b32_e32 v56, v58
	v_mov_b32_e32 v57, v62
	v_add_f32_e32 v50, 1.0, v50
	v_pk_mul_f32 v[52:53], v[56:57], v[52:53]
	v_rcp_f32_e32 v56, v50
	v_add_f32_e32 v50, 1.0, v54
	v_rcp_f32_e32 v57, v50
	v_pk_mul_f32 v[52:53], v[52:53], v[64:65] op_sel_hi:[1,0]
	v_mov_b32_e32 v54, v51
	v_cvt_pk_bf16_f32 v50, v52, v53
	v_pk_mul_f32 v[52:53], v[54:55], v[56:57]
	v_mov_b32_e32 v62, v59
	v_pk_mul_f32 v[52:53], v[62:63], v[52:53]
	v_lshlrev_b64 v[66:67], 10, v[208:209]
	v_pk_mul_f32 v[68:69], v[68:69], v[64:65] op_sel_hi:[1,0]
	v_pk_mul_f32 v[52:53], v[52:53], v[64:65] op_sel_hi:[1,0]
	v_lshl_add_u64 v[66:67], v[128:129], 0, v[66:67]
	v_cvt_pk_bf16_f32 v48, v68, v69
	v_cvt_pk_bf16_f32 v51, v52, v53
	global_store_dwordx4 v[66:67], v[48:51], off sc0 sc1
.LBB0_1166:
	s_or_b64 exec, exec, s[4:5]
	s_nop 0
	v_or_b32_e32 v48, 0x50, v130
	v_lshl_add_u32 v48, v48, 2, 0
	v_add_u32_e32 v49, 0x24200, v48
	ds_read_b32 v208, v49
	s_waitcnt lgkmcnt(0)
	v_cmp_lt_i32_e32 vcc, -1, v208
	s_and_saveexec_b64 s[4:5], vcc
	s_cbranch_execz .LBB0_1168
	v_mul_f32_e32 v49, 0xbfb8aa3b, v32
	v_exp_f32_e32 v49, v49
	v_mul_f32_e32 v50, 0xbfb8aa3b, v36
	v_exp_f32_e32 v53, v50
	v_mov_b32_e32 v54, v32
	v_add_f32_e32 v49, 1.0, v49
	v_rcp_f32_e32 v52, v49
	v_add_f32_e32 v49, 1.0, v53
	v_mul_f32_e32 v32, 0xbfb8aa3b, v33
	v_rcp_f32_e32 v53, v49
	v_mov_b32_e32 v55, v36
	v_exp_f32_e32 v32, v32
	v_mul_f32_e32 v36, 0xbfb8aa3b, v37
	v_exp_f32_e32 v36, v36
	v_pk_mul_f32 v[52:53], v[54:55], v[52:53]
	v_mov_b32_e32 v54, v40
	v_mov_b32_e32 v55, v44
	v_add_f32_e32 v32, 1.0, v32
	v_pk_mul_f32 v[52:53], v[54:55], v[52:53]
	v_rcp_f32_e32 v54, v32
	v_add_f32_e32 v32, 1.0, v36
	v_add_u32_e32 v48, 0x25a00, v48
	v_rcp_f32_e32 v55, v32
	v_mov_b32_e32 v36, v33
	v_mul_f32_e32 v33, 0xbfb8aa3b, v34
	ds_read_b32 v48, v48
	v_exp_f32_e32 v33, v33
	v_mul_f32_e32 v40, 0xbfb8aa3b, v38
	v_mov_b32_e32 v44, v41
	v_exp_f32_e32 v41, v40
	v_pk_mul_f32 v[36:37], v[36:37], v[54:55]
	v_add_f32_e32 v33, 1.0, v33
	v_pk_mul_f32 v[36:37], v[44:45], v[36:37]
	v_rcp_f32_e32 v40, v33
	s_waitcnt lgkmcnt(0)
	v_pk_mul_f32 v[36:37], v[36:37], v[48:49] op_sel_hi:[1,0]
	v_add_f32_e32 v33, 1.0, v41
	v_rcp_f32_e32 v41, v33
	v_cvt_pk_bf16_f32 v33, v36, v37
	v_mov_b32_e32 v36, v34
	v_mul_f32_e32 v34, 0xbfb8aa3b, v35
	v_mov_b32_e32 v37, v38
	v_exp_f32_e32 v34, v34
	v_mul_f32_e32 v38, 0xbfb8aa3b, v39
	v_exp_f32_e32 v38, v38
	v_pk_mul_f32 v[36:37], v[36:37], v[40:41]
	v_mov_b32_e32 v40, v42
	v_mov_b32_e32 v41, v46
	v_add_f32_e32 v34, 1.0, v34
	v_pk_mul_f32 v[36:37], v[40:41], v[36:37]
	v_rcp_f32_e32 v40, v34
	v_add_f32_e32 v34, 1.0, v38
	v_rcp_f32_e32 v41, v34
	v_pk_mul_f32 v[36:37], v[36:37], v[48:49] op_sel_hi:[1,0]
	v_mov_b32_e32 v38, v35
	v_cvt_pk_bf16_f32 v34, v36, v37
	v_pk_mul_f32 v[36:37], v[38:39], v[40:41]
	v_mov_b32_e32 v46, v43
	v_pk_mul_f32 v[36:37], v[46:47], v[36:37]
	v_lshlrev_b64 v[50:51], 10, v[208:209]
	v_pk_mul_f32 v[52:53], v[52:53], v[48:49] op_sel_hi:[1,0]
	v_pk_mul_f32 v[36:37], v[36:37], v[48:49] op_sel_hi:[1,0]
	v_lshl_add_u64 v[50:51], v[128:129], 0, v[50:51]
	v_cvt_pk_bf16_f32 v32, v52, v53
	v_cvt_pk_bf16_f32 v35, v36, v37
	global_store_dwordx4 v[50:51], v[32:35], off sc0 sc1
.LBB0_1168:
	s_or_b64 exec, exec, s[4:5]
	s_nop 0
	v_or_b32_e32 v32, 0x60, v130
	v_lshl_add_u32 v32, v32, 2, 0
	v_add_u32_e32 v33, 0x24200, v32
	ds_read_b32 v208, v33
	s_waitcnt lgkmcnt(0)
	v_cmp_lt_i32_e32 vcc, -1, v208
	s_and_saveexec_b64 s[4:5], vcc
	s_cbranch_execz .LBB0_1170
	v_mul_f32_e32 v33, 0xbfb8aa3b, v16
	v_exp_f32_e32 v33, v33
	v_mul_f32_e32 v34, 0xbfb8aa3b, v20
	v_exp_f32_e32 v37, v34
	v_mov_b32_e32 v38, v16
	v_add_f32_e32 v33, 1.0, v33
	v_rcp_f32_e32 v36, v33
	v_add_f32_e32 v33, 1.0, v37
	v_mul_f32_e32 v16, 0xbfb8aa3b, v17
	v_rcp_f32_e32 v37, v33
	v_mov_b32_e32 v39, v20
	v_exp_f32_e32 v16, v16
	v_mul_f32_e32 v20, 0xbfb8aa3b, v21
	v_exp_f32_e32 v20, v20
	v_pk_mul_f32 v[36:37], v[38:39], v[36:37]
	v_mov_b32_e32 v38, v24
	v_mov_b32_e32 v39, v28
	v_add_f32_e32 v16, 1.0, v16
	v_pk_mul_f32 v[36:37], v[38:39], v[36:37]
	v_rcp_f32_e32 v38, v16
	v_add_f32_e32 v16, 1.0, v20
	v_add_u32_e32 v32, 0x25a00, v32
	v_rcp_f32_e32 v39, v16
	v_mov_b32_e32 v20, v17
	v_mul_f32_e32 v17, 0xbfb8aa3b, v18
	ds_read_b32 v32, v32
	v_exp_f32_e32 v17, v17
	v_mul_f32_e32 v24, 0xbfb8aa3b, v22
	v_mov_b32_e32 v28, v25
	v_exp_f32_e32 v25, v24
	v_pk_mul_f32 v[20:21], v[20:21], v[38:39]
	v_add_f32_e32 v17, 1.0, v17
	v_pk_mul_f32 v[20:21], v[28:29], v[20:21]
	v_rcp_f32_e32 v24, v17
	s_waitcnt lgkmcnt(0)
	v_pk_mul_f32 v[20:21], v[20:21], v[32:33] op_sel_hi:[1,0]
	v_add_f32_e32 v17, 1.0, v25
	v_rcp_f32_e32 v25, v17
	v_cvt_pk_bf16_f32 v17, v20, v21
	v_mov_b32_e32 v20, v18
	v_mul_f32_e32 v18, 0xbfb8aa3b, v19
	v_mov_b32_e32 v21, v22
	v_exp_f32_e32 v18, v18
	v_mul_f32_e32 v22, 0xbfb8aa3b, v23
	v_exp_f32_e32 v22, v22
	v_pk_mul_f32 v[20:21], v[20:21], v[24:25]
	v_mov_b32_e32 v24, v26
	v_mov_b32_e32 v25, v30
	v_add_f32_e32 v18, 1.0, v18
	v_pk_mul_f32 v[20:21], v[24:25], v[20:21]
	v_rcp_f32_e32 v24, v18
	v_add_f32_e32 v18, 1.0, v22
	v_rcp_f32_e32 v25, v18
	v_pk_mul_f32 v[20:21], v[20:21], v[32:33] op_sel_hi:[1,0]
	v_mov_b32_e32 v22, v19
	v_cvt_pk_bf16_f32 v18, v20, v21
	v_pk_mul_f32 v[20:21], v[22:23], v[24:25]
	v_mov_b32_e32 v30, v27
	v_pk_mul_f32 v[20:21], v[30:31], v[20:21]
	v_lshlrev_b64 v[34:35], 10, v[208:209]
	v_pk_mul_f32 v[36:37], v[36:37], v[32:33] op_sel_hi:[1,0]
	v_pk_mul_f32 v[20:21], v[20:21], v[32:33] op_sel_hi:[1,0]
	v_lshl_add_u64 v[34:35], v[128:129], 0, v[34:35]
	v_cvt_pk_bf16_f32 v16, v36, v37
	v_cvt_pk_bf16_f32 v19, v20, v21
	global_store_dwordx4 v[34:35], v[16:19], off sc0 sc1
.LBB0_1170:
	s_or_b64 exec, exec, s[4:5]
	s_nop 0
	v_or_b32_e32 v16, 0x70, v130
	v_lshl_add_u32 v16, v16, 2, 0
	v_add_u32_e32 v17, 0x24200, v16
	ds_read_b32 v208, v17
	s_waitcnt lgkmcnt(0)
	v_cmp_lt_i32_e32 vcc, -1, v208
	s_and_saveexec_b64 s[4:5], vcc
	s_cbranch_execz .LBB0_1172
	v_mul_f32_e32 v17, 0xbfb8aa3b, v0
	v_exp_f32_e32 v17, v17
	v_add_u32_e32 v16, 0x25a00, v16
	ds_read_b32 v16, v16
	v_mov_b32_e32 v23, v4
	v_add_f32_e32 v17, 1.0, v17
	v_rcp_f32_e32 v20, v17
	v_mul_f32_e32 v17, 0xbfb8aa3b, v4
	v_exp_f32_e32 v17, v17
	v_mul_f32_e32 v4, 0xbfb8aa3b, v1
	v_exp_f32_e32 v4, v4
	v_mov_b32_e32 v22, v0
	v_add_f32_e32 v17, 1.0, v17
	v_rcp_f32_e32 v21, v17
	v_add_f32_e32 v4, 1.0, v4
	v_lshlrev_b64 v[18:19], 10, v[208:209]
	v_lshl_add_u64 v[18:19], v[128:129], 0, v[18:19]
	v_pk_mul_f32 v[20:21], v[22:23], v[20:21]
	v_mov_b32_e32 v22, v8
	v_mov_b32_e32 v23, v12
	v_pk_mul_f32 v[20:21], v[22:23], v[20:21]
	v_mov_b32_e32 v12, v9
	s_waitcnt lgkmcnt(0)
	v_pk_mul_f32 v[20:21], v[20:21], v[16:17] op_sel_hi:[1,0]
	v_mov_b32_e32 v8, v2
	v_cvt_pk_bf16_f32 v0, v20, v21
	v_rcp_f32_e32 v20, v4
	v_mul_f32_e32 v4, 0xbfb8aa3b, v5
	v_exp_f32_e32 v4, v4
	v_mov_b32_e32 v9, v6
	v_add_f32_e32 v4, 1.0, v4
	v_rcp_f32_e32 v21, v4
	v_mov_b32_e32 v4, v1
	v_pk_mul_f32 v[4:5], v[4:5], v[20:21]
	s_nop 0
	v_pk_mul_f32 v[4:5], v[12:13], v[4:5]
	s_nop 0
	v_pk_mul_f32 v[4:5], v[4:5], v[16:17] op_sel_hi:[1,0]
	s_nop 0
	v_cvt_pk_bf16_f32 v1, v4, v5
	v_mul_f32_e32 v4, 0xbfb8aa3b, v2
	v_mul_f32_e32 v5, 0xbfb8aa3b, v6
	v_exp_f32_e32 v4, v4
	v_exp_f32_e32 v5, v5
	v_mov_b32_e32 v6, v3
	v_add_f32_e32 v4, 1.0, v4
	v_add_f32_e32 v5, 1.0, v5
	v_rcp_f32_e32 v4, v4
	v_rcp_f32_e32 v5, v5
	s_nop 0
	v_pk_mul_f32 v[4:5], v[8:9], v[4:5]
	v_mov_b32_e32 v8, v10
	v_mov_b32_e32 v9, v14
	v_pk_mul_f32 v[4:5], v[8:9], v[4:5]
	v_mov_b32_e32 v14, v11
	v_pk_mul_f32 v[4:5], v[4:5], v[16:17] op_sel_hi:[1,0]
	s_nop 0
	v_cvt_pk_bf16_f32 v2, v4, v5
	v_mul_f32_e32 v4, 0xbfb8aa3b, v3
	v_mul_f32_e32 v5, 0xbfb8aa3b, v7
	v_exp_f32_e32 v4, v4
	v_exp_f32_e32 v5, v5
	v_add_f32_e32 v4, 1.0, v4
	v_add_f32_e32 v5, 1.0, v5
	v_rcp_f32_e32 v4, v4
	v_rcp_f32_e32 v5, v5
	s_nop 0
	v_pk_mul_f32 v[4:5], v[6:7], v[4:5]
	s_nop 0
	v_pk_mul_f32 v[4:5], v[14:15], v[4:5]
	s_nop 0
	v_pk_mul_f32 v[4:5], v[4:5], v[16:17] op_sel_hi:[1,0]
	s_nop 0
	v_cvt_pk_bf16_f32 v3, v4, v5
	global_store_dwordx4 v[18:19], v[0:3], off sc0 sc1
.LBB0_1172:
	s_or_b64 exec, exec, s[4:5]
	s_waitcnt vmcnt(0)
	s_waitcnt vmcnt(0)
	s_barrier
	s_and_saveexec_b64 s[4:5], s[2:3]
	s_cbranch_execz .LBB0_1143
	s_mov_b64 s[6:7], exec
	v_mbcnt_lo_u32_b32 v0, s6, 0
	s_waitcnt vmcnt(0)
	v_mbcnt_hi_u32_b32 v0, s7, v0
	v_cmp_eq_u32_e32 vcc, 0, v0
	s_and_b64 s[18:19], exec, vcc
	s_mov_b64 exec, s[18:19]
	s_cbranch_execz .LBB0_1143
	v_mov_b32_e32 v0, s30
	ds_read2_b32 v[0:1], v0 offset1:1
	s_waitcnt lgkmcnt(0)
	v_readfirstlane_b32 s18, v0
	v_readfirstlane_b32 s19, v1
	s_lshl_b32 s18, s18, 9
	s_lshl_b32 s19, s19, 4
	s_add_i32 s18, s19, s18
	s_ashr_i32 s19, s18, 31
	s_lshl_b64 s[18:19], s[18:19], 2
	s_add_u32 s18, s20, s18
	s_addc_u32 s19, s21, s19
	s_bcnt1_i32_b64 s6, s[6:7]
	v_mov_b32_e32 v0, s6
	global_atomic_add v209, v0, s[18:19]
	s_branch .LBB0_1143

.LBB0_1181:
	s_sub_i32 s19, s23, s24
	s_cmp_gt_i32 s19, -1
	s_cselect_b64 s[6:7], -1, 0
	s_cmp_lt_i32 s19, 0
	s_cselect_b64 s[4:5], -1, 0
	v_cmp_ge_i32_e32 vcc, s19, v0
	s_or_b64 s[4:5], s[4:5], vcc
	s_and_b64 vcc, exec, s[4:5]
	s_cbranch_vccnz .LBB0_1190
	s_movk_i32 s4, 0x100
	v_cmp_gt_i32_e32 vcc, s4, v206
	s_and_saveexec_b64 s[4:5], vcc
	s_cbranch_execz .LBB0_1189
	v_readlane_b32 s16, v255, 4
	v_mov_b32_e32 v208, -1
	s_nop 0
	v_readlane_b32 s100, v255, 4
	s_nop 1
	v_mov_b32_e32 v214, s100
	ds_read2_b32 v[128:129], v214 offset1:1
	v_readlane_b32 s100, v254, 45
	s_nop 1
	v_mov_b32_e32 v214, s100
	ds_read2_b32 v[130:131], v214 offset1:1
	v_readlane_b32 s100, v254, 47
	s_nop 1
	v_mov_b32_e32 v214, s100
	ds_read2_b32 v[132:133], v214 offset1:1
	v_readlane_b32 s100, v254, 48
	s_nop 1
	v_mov_b32_e32 v214, s100
	ds_read2_b32 v[134:135], v214 offset1:1
	v_readlane_b32 s100, v254, 50
	s_nop 1
	v_mov_b32_e32 v214, s100
	ds_read2_b32 v[136:137], v214 offset1:1
	v_readlane_b32 s100, v254, 51
	s_nop 1
	v_mov_b32_e32 v214, s100
	ds_read2_b32 v[138:139], v214 offset1:1
	v_readlane_b32 s100, v254, 53
	s_nop 1
	v_mov_b32_e32 v214, s100
	ds_read2_b32 v[140:141], v214 offset1:1
	v_readlane_b32 s100, v254, 54
	s_nop 1
	v_mov_b32_e32 v214, s100
	ds_read2_b32 v[142:143], v214 offset1:1
	s_waitcnt lgkmcnt(0)
	v_readlane_b32 s100, v254, 56
	s_nop 1
	v_mov_b32_e32 v214, s100
	ds_read2_b32 v[144:145], v214 offset1:1
	v_readlane_b32 s100, v254, 57
	s_nop 1
	v_mov_b32_e32 v214, s100
	ds_read2_b32 v[146:147], v214 offset1:1
	v_readlane_b32 s100, v254, 59
	s_nop 1
	v_mov_b32_e32 v214, s100
	ds_read2_b32 v[148:149], v214 offset1:1
	v_readlane_b32 s100, v254, 60
	s_nop 1
	v_mov_b32_e32 v214, s100
	ds_read2_b32 v[150:151], v214 offset1:1
	v_readlane_b32 s100, v254, 62
	s_nop 1
	v_mov_b32_e32 v214, s100
	ds_read2_b32 v[152:153], v214 offset1:1
	v_readlane_b32 s100, v254, 63
	s_nop 1
	v_mov_b32_e32 v214, s100
	ds_read2_b32 v[154:155], v214 offset1:1
	v_readlane_b32 s100, v255, 1
	s_nop 1
	v_mov_b32_e32 v214, s100
	ds_read2_b32 v[156:157], v214 offset1:1
	s_waitcnt lgkmcnt(0)
	v_mov_b32_e32 v0, v128
	v_mov_b32_e32 v1, v129
	v_readlane_b32 s16, v254, 45
	s_waitcnt lgkmcnt(0)
	v_cmp_ge_i32_e32 vcc, s19, v0
	s_nop 1
	v_cndmask_b32_e64 v0, 0, 1, vcc
	v_cmp_lt_i32_e32 vcc, s19, v1
	s_nop 1
	v_cndmask_b32_e32 v2, 2, v0, vcc
	v_mov_b32_e32 v0, v130
	v_mov_b32_e32 v1, v131
	v_readlane_b32 s16, v254, 47
	s_waitcnt lgkmcnt(0)
	v_cmp_lt_i32_e32 vcc, s19, v0
	s_nop 1
	v_cndmask_b32_e32 v0, 3, v2, vcc
	v_cmp_lt_i32_e32 vcc, s19, v1
	s_nop 1
	v_cndmask_b32_e32 v2, 4, v0, vcc
	v_mov_b32_e32 v0, v132
	v_mov_b32_e32 v1, v133
	v_readlane_b32 s16, v254, 48
	s_waitcnt lgkmcnt(0)
	v_cmp_lt_i32_e32 vcc, s19, v0
	s_nop 1
	v_cndmask_b32_e32 v0, 5, v2, vcc
	v_cmp_lt_i32_e32 vcc, s19, v1
	s_nop 1
	v_cndmask_b32_e32 v2, 6, v0, vcc
	v_mov_b32_e32 v0, v134
	v_mov_b32_e32 v1, v135
	v_readlane_b32 s16, v254, 50
	s_waitcnt lgkmcnt(0)
	v_cmp_lt_i32_e32 vcc, s19, v0
	s_nop 1
	v_cndmask_b32_e32 v0, 7, v2, vcc
	v_cmp_lt_i32_e32 vcc, s19, v1
	s_nop 1
	v_cndmask_b32_e32 v2, 8, v0, vcc
	v_mov_b32_e32 v0, v136
	v_mov_b32_e32 v1, v137
	v_readlane_b32 s16, v254, 51
	s_waitcnt lgkmcnt(0)
	v_cmp_lt_i32_e32 vcc, s19, v0
	s_nop 1
	v_cndmask_b32_e32 v0, 9, v2, vcc
	v_cmp_lt_i32_e32 vcc, s19, v1
	s_nop 1
	v_cndmask_b32_e32 v2, 10, v0, vcc
	v_mov_b32_e32 v0, v138
	v_mov_b32_e32 v1, v139
	v_readlane_b32 s16, v254, 53
	s_waitcnt lgkmcnt(0)
	v_cmp_lt_i32_e32 vcc, s19, v0
	s_nop 1
	v_cndmask_b32_e32 v0, 11, v2, vcc
	v_cmp_lt_i32_e32 vcc, s19, v1
	s_nop 1
	v_cndmask_b32_e32 v2, 12, v0, vcc
	v_mov_b32_e32 v0, v140
	v_mov_b32_e32 v1, v141
	v_readlane_b32 s16, v254, 54
	s_waitcnt lgkmcnt(0)
	v_cmp_lt_i32_e32 vcc, s19, v0
	s_nop 1
	v_cndmask_b32_e32 v0, 13, v2, vcc
	v_cmp_lt_i32_e32 vcc, s19, v1
	s_nop 1
	v_cndmask_b32_e32 v2, 14, v0, vcc
	v_mov_b32_e32 v0, v142
	v_mov_b32_e32 v1, v143
	v_readlane_b32 s16, v254, 56
	s_waitcnt lgkmcnt(0)
	v_cmp_lt_i32_e32 vcc, s19, v0
	s_nop 1
	v_cndmask_b32_e32 v0, 15, v2, vcc
	v_cmp_lt_i32_e32 vcc, s19, v1
	s_nop 1
	v_cndmask_b32_e32 v2, 16, v0, vcc
	v_mov_b32_e32 v0, v144
	v_mov_b32_e32 v1, v145
	v_readlane_b32 s16, v254, 57
	s_waitcnt lgkmcnt(0)
	v_cmp_lt_i32_e32 vcc, s19, v0
	s_nop 1
	v_cndmask_b32_e32 v0, 17, v2, vcc
	v_cmp_lt_i32_e32 vcc, s19, v1
	s_nop 1
	v_cndmask_b32_e32 v2, 18, v0, vcc
	v_mov_b32_e32 v0, v146
	v_mov_b32_e32 v1, v147
	v_readlane_b32 s16, v254, 59
	s_waitcnt lgkmcnt(0)
	v_cmp_lt_i32_e32 vcc, s19, v0
	s_nop 1
	v_cndmask_b32_e32 v0, 19, v2, vcc
	v_cmp_lt_i32_e32 vcc, s19, v1
	s_nop 1
	v_cndmask_b32_e32 v2, 20, v0, vcc
	v_mov_b32_e32 v0, v148
	v_mov_b32_e32 v1, v149
	v_readlane_b32 s16, v254, 60
	s_waitcnt lgkmcnt(0)
	v_cmp_lt_i32_e32 vcc, s19, v0
	s_nop 1
	v_cndmask_b32_e32 v0, 21, v2, vcc
	v_cmp_lt_i32_e32 vcc, s19, v1
	s_nop 1
	v_cndmask_b32_e32 v2, 22, v0, vcc
	v_mov_b32_e32 v0, v150
	v_mov_b32_e32 v1, v151
	v_readlane_b32 s16, v254, 62
	s_waitcnt lgkmcnt(0)
	v_cmp_lt_i32_e32 vcc, s19, v0
	s_nop 1
	v_cndmask_b32_e32 v0, 23, v2, vcc
	v_cmp_lt_i32_e32 vcc, s19, v1
	s_nop 1
	v_cndmask_b32_e32 v2, 24, v0, vcc
	v_mov_b32_e32 v0, v152
	v_mov_b32_e32 v1, v153
	v_readlane_b32 s16, v254, 63
	s_waitcnt lgkmcnt(0)
	v_cmp_lt_i32_e32 vcc, s19, v0
	s_nop 1
	v_cndmask_b32_e32 v0, 25, v2, vcc
	v_cmp_lt_i32_e32 vcc, s19, v1
	s_nop 1
	v_cndmask_b32_e32 v2, 26, v0, vcc
	v_mov_b32_e32 v0, v154
	v_mov_b32_e32 v1, v155
	v_readlane_b32 s16, v255, 1
	s_waitcnt lgkmcnt(0)
	v_cmp_lt_i32_e32 vcc, s19, v0
	s_nop 1
	v_cndmask_b32_e32 v0, 27, v2, vcc
	v_cmp_lt_i32_e32 vcc, s19, v1
	s_nop 1
	v_cndmask_b32_e32 v2, 28, v0, vcc
	v_mov_b32_e32 v0, v156
	v_mov_b32_e32 v1, v157
	v_readlane_b32 s16, v255, 2
	s_waitcnt lgkmcnt(0)
	v_cmp_lt_i32_e32 vcc, s19, v0
	s_nop 1
	v_cndmask_b32_e32 v0, 29, v2, vcc
	v_cmp_lt_i32_e32 vcc, s19, v1
	v_mov_b32_e32 v1, s16
	ds_read_b32 v1, v1
	v_cndmask_b32_e32 v0, 30, v0, vcc
	s_waitcnt lgkmcnt(0)
	v_cmp_lt_i32_e32 vcc, s19, v1
	s_nop 1
	v_cndmask_b32_e32 v0, 31, v0, vcc
	v_lshlrev_b32_e32 v1, 2, v0
	v_add_u32_e32 v1, 0, v1
	v_add_u32_e32 v2, 0x24000, v1
	ds_read_b32 v2, v2
	v_add_u32_e32 v1, 0x24100, v1
	ds_read_b32 v1, v1
	s_waitcnt lgkmcnt(1)
	v_readfirstlane_b32 s16, v2
	s_addk_i32 s16, 0xff
	s_ashr_i32 s16, s16, 8
	s_abs_i32 s25, s16
	s_waitcnt lgkmcnt(0)
	v_readfirstlane_b32 s17, v1
	v_cvt_f32_u32_e32 v1, s25
	s_sub_i32 s26, 0, s25
	s_sub_i32 s17, s19, s17
	s_abs_i32 s23, s17
	v_rcp_iflag_f32_e32 v1, v1
	s_xor_b32 s18, s17, s16
	s_ashr_i32 s18, s18, 31
	v_mul_f32_e32 v1, 0x4f7ffffe, v1
	v_cvt_u32_f32_e32 v1, v1
	s_nop 0
	v_readfirstlane_b32 s27, v1
	s_mul_i32 s26, s26, s27
	s_mul_hi_u32 s26, s27, s26
	s_add_i32 s27, s27, s26
	s_mul_hi_u32 s26, s23, s27
	s_mul_i32 s27, s26, s25
	s_sub_i32 s23, s23, s27
	s_add_i32 s27, s26, 1
	s_sub_i32 s28, s23, s25
	s_cmp_ge_u32 s23, s25
	s_cselect_b32 s26, s27, s26
	s_cselect_b32 s23, s28, s23
	s_add_i32 s27, s26, 1
	s_cmp_ge_u32 s23, s25
	s_cselect_b32 s23, s27, s26
	s_xor_b32 s23, s23, s18
	s_sub_i32 s18, s23, s18
	s_mul_i32 s16, s18, s16
	s_sub_i32 s23, s17, s16
	v_lshl_add_u32 v1, s23, 8, v206
	v_cmp_lt_i32_e32 vcc, v1, v2
	s_and_saveexec_b64 s[16:17], vcc
	s_cbranch_execz .LBB0_1185
	v_lshl_add_u32 v2, v0, 13, v1
	v_ashrrev_i32_e32 v3, 31, v2
	v_lshl_add_u64 v[2:3], v[2:3], 2, s[14:15]
	global_load_dword v208, v[2:3], off

.LBB0_1190:
	v_cndmask_b32_e64 v0, 0, 1, s[6:7]
	v_cmp_ne_u32_e64 s[4:5], 1, v0
	s_andn2_b64 vcc, exec, s[6:7]
	s_sub_i32 s22, s22, s24
	s_cbranch_vccnz .LBB0_1200
	v_readlane_b32 s6, v255, 3
	s_add_i32 s16, s22, s19
	s_nop 0
	v_mov_b32_e32 v0, s6
	ds_read_b32 v0, v0
	s_waitcnt lgkmcnt(0)
	v_cmp_ge_i32_e32 vcc, s16, v0
	s_cbranch_vccnz .LBB0_1200
	s_movk_i32 s6, 0x100
	v_cmp_gt_i32_e32 vcc, s6, v206
	s_and_saveexec_b64 s[6:7], vcc
	s_cbranch_execz .LBB0_1199
	v_readlane_b32 s17, v255, 4
	v_mov_b32_e32 v208, -1
	s_nop 0
	v_readlane_b32 s100, v255, 4
	s_nop 1
	v_mov_b32_e32 v214, s100
	ds_read2_b32 v[128:129], v214 offset1:1
	v_readlane_b32 s100, v254, 45
	s_nop 1
	v_mov_b32_e32 v214, s100
	ds_read2_b32 v[130:131], v214 offset1:1
	v_readlane_b32 s100, v254, 47
	s_nop 1
	v_mov_b32_e32 v214, s100
	ds_read2_b32 v[132:133], v214 offset1:1
	v_readlane_b32 s100, v254, 48
	s_nop 1
	v_mov_b32_e32 v214, s100
	ds_read2_b32 v[134:135], v214 offset1:1
	v_readlane_b32 s100, v254, 50
	s_nop 1
	v_mov_b32_e32 v214, s100
	ds_read2_b32 v[136:137], v214 offset1:1
	v_readlane_b32 s100, v254, 51
	s_nop 1
	v_mov_b32_e32 v214, s100
	ds_read2_b32 v[138:139], v214 offset1:1
	v_readlane_b32 s100, v254, 53
	s_nop 1
	v_mov_b32_e32 v214, s100
	ds_read2_b32 v[140:141], v214 offset1:1
	v_readlane_b32 s100, v254, 54
	s_nop 1
	v_mov_b32_e32 v214, s100
	ds_read2_b32 v[142:143], v214 offset1:1
	s_waitcnt lgkmcnt(0)
	v_readlane_b32 s100, v254, 56
	s_nop 1
	v_mov_b32_e32 v214, s100
	ds_read2_b32 v[144:145], v214 offset1:1
	v_readlane_b32 s100, v254, 57
	s_nop 1
	v_mov_b32_e32 v214, s100
	ds_read2_b32 v[146:147], v214 offset1:1
	v_readlane_b32 s100, v254, 59
	s_nop 1
	v_mov_b32_e32 v214, s100
	ds_read2_b32 v[148:149], v214 offset1:1
	v_readlane_b32 s100, v254, 60
	s_nop 1
	v_mov_b32_e32 v214, s100
	ds_read2_b32 v[150:151], v214 offset1:1
	v_readlane_b32 s100, v254, 62
	s_nop 1
	v_mov_b32_e32 v214, s100
	ds_read2_b32 v[152:153], v214 offset1:1
	v_readlane_b32 s100, v254, 63
	s_nop 1
	v_mov_b32_e32 v214, s100
	ds_read2_b32 v[154:155], v214 offset1:1
	v_readlane_b32 s100, v255, 1
	s_nop 1
	v_mov_b32_e32 v214, s100
	ds_read2_b32 v[156:157], v214 offset1:1
	s_waitcnt lgkmcnt(0)
	v_mov_b32_e32 v0, v128
	v_mov_b32_e32 v1, v129
	v_readlane_b32 s17, v254, 45
	s_waitcnt lgkmcnt(0)
	v_cmp_ge_i32_e32 vcc, s16, v0
	s_nop 1
	v_cndmask_b32_e64 v0, 0, 1, vcc
	v_cmp_lt_i32_e32 vcc, s16, v1
	s_nop 1
	v_cndmask_b32_e32 v2, 2, v0, vcc
	v_mov_b32_e32 v0, v130
	v_mov_b32_e32 v1, v131
	v_readlane_b32 s17, v254, 47
	s_waitcnt lgkmcnt(0)
	v_cmp_lt_i32_e32 vcc, s16, v0
	s_nop 1
	v_cndmask_b32_e32 v0, 3, v2, vcc
	v_cmp_lt_i32_e32 vcc, s16, v1
	s_nop 1
	v_cndmask_b32_e32 v2, 4, v0, vcc
	v_mov_b32_e32 v0, v132
	v_mov_b32_e32 v1, v133
	v_readlane_b32 s17, v254, 48
	s_waitcnt lgkmcnt(0)
	v_cmp_lt_i32_e32 vcc, s16, v0
	s_nop 1
	v_cndmask_b32_e32 v0, 5, v2, vcc
	v_cmp_lt_i32_e32 vcc, s16, v1
	s_nop 1
	v_cndmask_b32_e32 v2, 6, v0, vcc
	v_mov_b32_e32 v0, v134
	v_mov_b32_e32 v1, v135
	v_readlane_b32 s17, v254, 50
	s_waitcnt lgkmcnt(0)
	v_cmp_lt_i32_e32 vcc, s16, v0
	s_nop 1
	v_cndmask_b32_e32 v0, 7, v2, vcc
	v_cmp_lt_i32_e32 vcc, s16, v1
	s_nop 1
	v_cndmask_b32_e32 v2, 8, v0, vcc
	v_mov_b32_e32 v0, v136
	v_mov_b32_e32 v1, v137
	v_readlane_b32 s17, v254, 51
	s_waitcnt lgkmcnt(0)
	v_cmp_lt_i32_e32 vcc, s16, v0
	s_nop 1
	v_cndmask_b32_e32 v0, 9, v2, vcc
	v_cmp_lt_i32_e32 vcc, s16, v1
	s_nop 1
	v_cndmask_b32_e32 v2, 10, v0, vcc
	v_mov_b32_e32 v0, v138
	v_mov_b32_e32 v1, v139
	v_readlane_b32 s17, v254, 53
	s_waitcnt lgkmcnt(0)
	v_cmp_lt_i32_e32 vcc, s16, v0
	s_nop 1
	v_cndmask_b32_e32 v0, 11, v2, vcc
	v_cmp_lt_i32_e32 vcc, s16, v1
	s_nop 1
	v_cndmask_b32_e32 v2, 12, v0, vcc
	v_mov_b32_e32 v0, v140
	v_mov_b32_e32 v1, v141
	v_readlane_b32 s17, v254, 54
	s_waitcnt lgkmcnt(0)
	v_cmp_lt_i32_e32 vcc, s16, v0
	s_nop 1
	v_cndmask_b32_e32 v0, 13, v2, vcc
	v_cmp_lt_i32_e32 vcc, s16, v1
	s_nop 1
	v_cndmask_b32_e32 v2, 14, v0, vcc
	v_mov_b32_e32 v0, v142
	v_mov_b32_e32 v1, v143
	v_readlane_b32 s17, v254, 56
	s_waitcnt lgkmcnt(0)
	v_cmp_lt_i32_e32 vcc, s16, v0
	s_nop 1
	v_cndmask_b32_e32 v0, 15, v2, vcc
	v_cmp_lt_i32_e32 vcc, s16, v1
	s_nop 1
	v_cndmask_b32_e32 v2, 16, v0, vcc
	v_mov_b32_e32 v0, v144
	v_mov_b32_e32 v1, v145
	v_readlane_b32 s17, v254, 57
	s_waitcnt lgkmcnt(0)
	v_cmp_lt_i32_e32 vcc, s16, v0
	s_nop 1
	v_cndmask_b32_e32 v0, 17, v2, vcc
	v_cmp_lt_i32_e32 vcc, s16, v1
	s_nop 1
	v_cndmask_b32_e32 v2, 18, v0, vcc
	v_mov_b32_e32 v0, v146
	v_mov_b32_e32 v1, v147
	v_readlane_b32 s17, v254, 59
	s_waitcnt lgkmcnt(0)
	v_cmp_lt_i32_e32 vcc, s16, v0
	s_nop 1
	v_cndmask_b32_e32 v0, 19, v2, vcc
	v_cmp_lt_i32_e32 vcc, s16, v1
	s_nop 1
	v_cndmask_b32_e32 v2, 20, v0, vcc
	v_mov_b32_e32 v0, v148
	v_mov_b32_e32 v1, v149
	v_readlane_b32 s17, v254, 60
	s_waitcnt lgkmcnt(0)
	v_cmp_lt_i32_e32 vcc, s16, v0
	s_nop 1
	v_cndmask_b32_e32 v0, 21, v2, vcc
	v_cmp_lt_i32_e32 vcc, s16, v1
	s_nop 1
	v_cndmask_b32_e32 v2, 22, v0, vcc
	v_mov_b32_e32 v0, v150
	v_mov_b32_e32 v1, v151
	v_readlane_b32 s17, v254, 62
	s_waitcnt lgkmcnt(0)
	v_cmp_lt_i32_e32 vcc, s16, v0
	s_nop 1
	v_cndmask_b32_e32 v0, 23, v2, vcc
	v_cmp_lt_i32_e32 vcc, s16, v1
	s_nop 1
	v_cndmask_b32_e32 v2, 24, v0, vcc
	v_mov_b32_e32 v0, v152
	v_mov_b32_e32 v1, v153
	v_readlane_b32 s17, v254, 63
	s_waitcnt lgkmcnt(0)
	v_cmp_lt_i32_e32 vcc, s16, v0
	s_nop 1
	v_cndmask_b32_e32 v0, 25, v2, vcc
	v_cmp_lt_i32_e32 vcc, s16, v1
	s_nop 1
	v_cndmask_b32_e32 v2, 26, v0, vcc
	v_mov_b32_e32 v0, v154
	v_mov_b32_e32 v1, v155
	v_readlane_b32 s17, v255, 1
	s_waitcnt lgkmcnt(0)
	v_cmp_lt_i32_e32 vcc, s16, v0
	s_nop 1
	v_cndmask_b32_e32 v0, 27, v2, vcc
	v_cmp_lt_i32_e32 vcc, s16, v1
	s_nop 1
	v_cndmask_b32_e32 v2, 28, v0, vcc
	v_mov_b32_e32 v0, v156
	v_mov_b32_e32 v1, v157
	v_readlane_b32 s17, v255, 2
	s_waitcnt lgkmcnt(0)
	v_cmp_lt_i32_e32 vcc, s16, v0
	s_nop 1
	v_cndmask_b32_e32 v0, 29, v2, vcc
	v_cmp_lt_i32_e32 vcc, s16, v1
	v_mov_b32_e32 v1, s17
	ds_read_b32 v1, v1
	v_cndmask_b32_e32 v0, 30, v0, vcc
	s_waitcnt lgkmcnt(0)
	v_cmp_lt_i32_e32 vcc, s16, v1
	s_nop 1
	v_cndmask_b32_e32 v0, 31, v0, vcc
	v_lshlrev_b32_e32 v1, 2, v0
	v_add_u32_e32 v1, 0, v1
	v_add_u32_e32 v2, 0x24000, v1
	ds_read_b32 v2, v2
	v_add_u32_e32 v1, 0x24100, v1
	ds_read_b32 v1, v1
	s_waitcnt lgkmcnt(1)
	v_readfirstlane_b32 s17, v2
	s_addk_i32 s17, 0xff
	s_ashr_i32 s17, s17, 8
	s_abs_i32 s25, s17
	s_waitcnt lgkmcnt(0)
	v_readfirstlane_b32 s23, v1
	v_cvt_f32_u32_e32 v1, s25
	s_sub_i32 s26, 0, s25
	s_sub_i32 s16, s16, s23
	s_abs_i32 s24, s16
	v_rcp_iflag_f32_e32 v1, v1
	s_xor_b32 s23, s16, s17
	s_ashr_i32 s23, s23, 31
	v_mul_f32_e32 v1, 0x4f7ffffe, v1
	v_cvt_u32_f32_e32 v1, v1
	s_nop 0
	v_readfirstlane_b32 s27, v1
	s_mul_i32 s26, s26, s27
	s_mul_hi_u32 s26, s27, s26
	s_add_i32 s27, s27, s26
	s_mul_hi_u32 s26, s24, s27
	s_mul_i32 s27, s26, s25
	s_sub_i32 s24, s24, s27
	s_add_i32 s27, s26, 1
	s_sub_i32 s28, s24, s25
	s_cmp_ge_u32 s24, s25
	s_cselect_b32 s26, s27, s26
	s_cselect_b32 s24, s28, s24
	s_add_i32 s27, s26, 1
	s_cmp_ge_u32 s24, s25
	s_cselect_b32 s24, s27, s26
	s_xor_b32 s24, s24, s23
	s_sub_i32 s23, s24, s23
	s_mul_i32 s17, s23, s17
	s_sub_i32 s24, s16, s17
	v_lshl_add_u32 v1, s24, 8, v206
	v_cmp_lt_i32_e32 vcc, v1, v2
	s_and_saveexec_b64 s[16:17], vcc
	s_cbranch_execz .LBB0_1195
	v_lshl_add_u32 v2, v0, 13, v1
	v_ashrrev_i32_e32 v3, 31, v2
	v_lshl_add_u64 v[2:3], v[2:3], 2, s[14:15]
	global_load_dword v208, v[2:3], off

.LBB0_1200:
	s_and_b64 vcc, exec, s[4:5]
	s_cbranch_vccnz .LBB0_1210
	v_readlane_b32 s6, v255, 3
	s_lshl_b32 s16, s22, 1
	s_add_i32 s16, s16, s19
	v_mov_b32_e32 v0, s6
	ds_read_b32 v0, v0
	s_waitcnt lgkmcnt(0)
	v_cmp_ge_i32_e32 vcc, s16, v0
	s_cbranch_vccnz .LBB0_1210
	s_movk_i32 s6, 0x100
	v_cmp_gt_i32_e32 vcc, s6, v206
	s_and_saveexec_b64 s[6:7], vcc
	s_cbranch_execz .LBB0_1209
	v_readlane_b32 s17, v255, 4
	v_mov_b32_e32 v208, -1
	s_nop 0
	v_readlane_b32 s100, v255, 4
	s_nop 1
	v_mov_b32_e32 v214, s100
	ds_read2_b32 v[128:129], v214 offset1:1
	v_readlane_b32 s100, v254, 45
	s_nop 1
	v_mov_b32_e32 v214, s100
	ds_read2_b32 v[130:131], v214 offset1:1
	v_readlane_b32 s100, v254, 47
	s_nop 1
	v_mov_b32_e32 v214, s100
	ds_read2_b32 v[132:133], v214 offset1:1
	v_readlane_b32 s100, v254, 48
	s_nop 1
	v_mov_b32_e32 v214, s100
	ds_read2_b32 v[134:135], v214 offset1:1
	v_readlane_b32 s100, v254, 50
	s_nop 1
	v_mov_b32_e32 v214, s100
	ds_read2_b32 v[136:137], v214 offset1:1
	v_readlane_b32 s100, v254, 51
	s_nop 1
	v_mov_b32_e32 v214, s100
	ds_read2_b32 v[138:139], v214 offset1:1
	v_readlane_b32 s100, v254, 53
	s_nop 1
	v_mov_b32_e32 v214, s100
	ds_read2_b32 v[140:141], v214 offset1:1
	v_readlane_b32 s100, v254, 54
	s_nop 1
	v_mov_b32_e32 v214, s100
	ds_read2_b32 v[142:143], v214 offset1:1
	s_waitcnt lgkmcnt(0)
	v_readlane_b32 s100, v254, 56
	s_nop 1
	v_mov_b32_e32 v214, s100
	ds_read2_b32 v[144:145], v214 offset1:1
	v_readlane_b32 s100, v254, 57
	s_nop 1
	v_mov_b32_e32 v214, s100
	ds_read2_b32 v[146:147], v214 offset1:1
	v_readlane_b32 s100, v254, 59
	s_nop 1
	v_mov_b32_e32 v214, s100
	ds_read2_b32 v[148:149], v214 offset1:1
	v_readlane_b32 s100, v254, 60
	s_nop 1
	v_mov_b32_e32 v214, s100
	ds_read2_b32 v[150:151], v214 offset1:1
	v_readlane_b32 s100, v254, 62
	s_nop 1
	v_mov_b32_e32 v214, s100
	ds_read2_b32 v[152:153], v214 offset1:1
	v_readlane_b32 s100, v254, 63
	s_nop 1
	v_mov_b32_e32 v214, s100
	ds_read2_b32 v[154:155], v214 offset1:1
	v_readlane_b32 s100, v255, 1
	s_nop 1
	v_mov_b32_e32 v214, s100
	ds_read2_b32 v[156:157], v214 offset1:1
	s_waitcnt lgkmcnt(0)
	v_mov_b32_e32 v0, v128
	v_mov_b32_e32 v1, v129
	v_readlane_b32 s17, v254, 45
	s_waitcnt lgkmcnt(0)
	v_cmp_ge_i32_e32 vcc, s16, v0
	s_nop 1
	v_cndmask_b32_e64 v0, 0, 1, vcc
	v_cmp_lt_i32_e32 vcc, s16, v1
	s_nop 1
	v_cndmask_b32_e32 v2, 2, v0, vcc
	v_mov_b32_e32 v0, v130
	v_mov_b32_e32 v1, v131
	v_readlane_b32 s17, v254, 47
	s_waitcnt lgkmcnt(0)
	v_cmp_lt_i32_e32 vcc, s16, v0
	s_nop 1
	v_cndmask_b32_e32 v0, 3, v2, vcc
	v_cmp_lt_i32_e32 vcc, s16, v1
	s_nop 1
	v_cndmask_b32_e32 v2, 4, v0, vcc
	v_mov_b32_e32 v0, v132
	v_mov_b32_e32 v1, v133
	v_readlane_b32 s17, v254, 48
	s_waitcnt lgkmcnt(0)
	v_cmp_lt_i32_e32 vcc, s16, v0
	s_nop 1
	v_cndmask_b32_e32 v0, 5, v2, vcc
	v_cmp_lt_i32_e32 vcc, s16, v1
	s_nop 1
	v_cndmask_b32_e32 v2, 6, v0, vcc
	v_mov_b32_e32 v0, v134
	v_mov_b32_e32 v1, v135
	v_readlane_b32 s17, v254, 50
	s_waitcnt lgkmcnt(0)
	v_cmp_lt_i32_e32 vcc, s16, v0
	s_nop 1
	v_cndmask_b32_e32 v0, 7, v2, vcc
	v_cmp_lt_i32_e32 vcc, s16, v1
	s_nop 1
	v_cndmask_b32_e32 v2, 8, v0, vcc
	v_mov_b32_e32 v0, v136
	v_mov_b32_e32 v1, v137
	v_readlane_b32 s17, v254, 51
	s_waitcnt lgkmcnt(0)
	v_cmp_lt_i32_e32 vcc, s16, v0
	s_nop 1
	v_cndmask_b32_e32 v0, 9, v2, vcc
	v_cmp_lt_i32_e32 vcc, s16, v1
	s_nop 1
	v_cndmask_b32_e32 v2, 10, v0, vcc
	v_mov_b32_e32 v0, v138
	v_mov_b32_e32 v1, v139
	v_readlane_b32 s17, v254, 53
	s_waitcnt lgkmcnt(0)
	v_cmp_lt_i32_e32 vcc, s16, v0
	s_nop 1
	v_cndmask_b32_e32 v0, 11, v2, vcc
	v_cmp_lt_i32_e32 vcc, s16, v1
	s_nop 1
	v_cndmask_b32_e32 v2, 12, v0, vcc
	v_mov_b32_e32 v0, v140
	v_mov_b32_e32 v1, v141
	v_readlane_b32 s17, v254, 54
	s_waitcnt lgkmcnt(0)
	v_cmp_lt_i32_e32 vcc, s16, v0
	s_nop 1
	v_cndmask_b32_e32 v0, 13, v2, vcc
	v_cmp_lt_i32_e32 vcc, s16, v1
	s_nop 1
	v_cndmask_b32_e32 v2, 14, v0, vcc
	v_mov_b32_e32 v0, v142
	v_mov_b32_e32 v1, v143
	v_readlane_b32 s17, v254, 56
	s_waitcnt lgkmcnt(0)
	v_cmp_lt_i32_e32 vcc, s16, v0
	s_nop 1
	v_cndmask_b32_e32 v0, 15, v2, vcc
	v_cmp_lt_i32_e32 vcc, s16, v1
	s_nop 1
	v_cndmask_b32_e32 v2, 16, v0, vcc
	v_mov_b32_e32 v0, v144
	v_mov_b32_e32 v1, v145
	v_readlane_b32 s17, v254, 57
	s_waitcnt lgkmcnt(0)
	v_cmp_lt_i32_e32 vcc, s16, v0
	s_nop 1
	v_cndmask_b32_e32 v0, 17, v2, vcc
	v_cmp_lt_i32_e32 vcc, s16, v1
	s_nop 1
	v_cndmask_b32_e32 v2, 18, v0, vcc
	v_mov_b32_e32 v0, v146
	v_mov_b32_e32 v1, v147
	v_readlane_b32 s17, v254, 59
	s_waitcnt lgkmcnt(0)
	v_cmp_lt_i32_e32 vcc, s16, v0
	s_nop 1
	v_cndmask_b32_e32 v0, 19, v2, vcc
	v_cmp_lt_i32_e32 vcc, s16, v1
	s_nop 1
	v_cndmask_b32_e32 v2, 20, v0, vcc
	v_mov_b32_e32 v0, v148
	v_mov_b32_e32 v1, v149
	v_readlane_b32 s17, v254, 60
	s_waitcnt lgkmcnt(0)
	v_cmp_lt_i32_e32 vcc, s16, v0
	s_nop 1
	v_cndmask_b32_e32 v0, 21, v2, vcc
	v_cmp_lt_i32_e32 vcc, s16, v1
	s_nop 1
	v_cndmask_b32_e32 v2, 22, v0, vcc
	v_mov_b32_e32 v0, v150
	v_mov_b32_e32 v1, v151
	v_readlane_b32 s17, v254, 62
	s_waitcnt lgkmcnt(0)
	v_cmp_lt_i32_e32 vcc, s16, v0
	s_nop 1
	v_cndmask_b32_e32 v0, 23, v2, vcc
	v_cmp_lt_i32_e32 vcc, s16, v1
	s_nop 1
	v_cndmask_b32_e32 v2, 24, v0, vcc
	v_mov_b32_e32 v0, v152
	v_mov_b32_e32 v1, v153
	v_readlane_b32 s17, v254, 63
	s_waitcnt lgkmcnt(0)
	v_cmp_lt_i32_e32 vcc, s16, v0
	s_nop 1
	v_cndmask_b32_e32 v0, 25, v2, vcc
	v_cmp_lt_i32_e32 vcc, s16, v1
	s_nop 1
	v_cndmask_b32_e32 v2, 26, v0, vcc
	v_mov_b32_e32 v0, v154
	v_mov_b32_e32 v1, v155
	v_readlane_b32 s17, v255, 1
	s_waitcnt lgkmcnt(0)
	v_cmp_lt_i32_e32 vcc, s16, v0
	s_nop 1
	v_cndmask_b32_e32 v0, 27, v2, vcc
	v_cmp_lt_i32_e32 vcc, s16, v1
	s_nop 1
	v_cndmask_b32_e32 v2, 28, v0, vcc
	v_mov_b32_e32 v0, v156
	v_mov_b32_e32 v1, v157
	v_readlane_b32 s17, v255, 2
	s_waitcnt lgkmcnt(0)
	v_cmp_lt_i32_e32 vcc, s16, v0
	s_nop 1
	v_cndmask_b32_e32 v0, 29, v2, vcc
	v_cmp_lt_i32_e32 vcc, s16, v1
	v_mov_b32_e32 v1, s17
	ds_read_b32 v1, v1
	v_cndmask_b32_e32 v0, 30, v0, vcc
	s_waitcnt lgkmcnt(0)
	v_cmp_lt_i32_e32 vcc, s16, v1
	s_nop 1
	v_cndmask_b32_e32 v0, 31, v0, vcc
	v_lshlrev_b32_e32 v1, 2, v0
	v_add_u32_e32 v1, 0, v1
	v_add_u32_e32 v2, 0x24000, v1
	ds_read_b32 v2, v2
	v_add_u32_e32 v1, 0x24100, v1
	ds_read_b32 v1, v1
	s_waitcnt lgkmcnt(1)
	v_readfirstlane_b32 s17, v2
	s_addk_i32 s17, 0xff
	s_ashr_i32 s17, s17, 8
	s_abs_i32 s25, s17
	s_waitcnt lgkmcnt(0)
	v_readfirstlane_b32 s23, v1
	v_cvt_f32_u32_e32 v1, s25
	s_sub_i32 s26, 0, s25
	s_sub_i32 s16, s16, s23
	s_abs_i32 s24, s16
	v_rcp_iflag_f32_e32 v1, v1
	s_xor_b32 s23, s16, s17
	s_ashr_i32 s23, s23, 31
	v_mul_f32_e32 v1, 0x4f7ffffe, v1
	v_cvt_u32_f32_e32 v1, v1
	s_nop 0
	v_readfirstlane_b32 s27, v1
	s_mul_i32 s26, s26, s27
	s_mul_hi_u32 s26, s27, s26
	s_add_i32 s27, s27, s26
	s_mul_hi_u32 s26, s24, s27
	s_mul_i32 s27, s26, s25
	s_sub_i32 s24, s24, s27
	s_add_i32 s27, s26, 1
	s_sub_i32 s28, s24, s25
	s_cmp_ge_u32 s24, s25
	s_cselect_b32 s26, s27, s26
	s_cselect_b32 s24, s28, s24
	s_add_i32 s27, s26, 1
	s_cmp_ge_u32 s24, s25
	s_cselect_b32 s24, s27, s26
	s_xor_b32 s24, s24, s23
	s_sub_i32 s23, s24, s23
	s_mul_i32 s17, s23, s17
	s_sub_i32 s24, s16, s17
	v_lshl_add_u32 v1, s24, 8, v206
	v_cmp_lt_i32_e32 vcc, v1, v2
	s_and_saveexec_b64 s[16:17], vcc
	s_cbranch_execz .LBB0_1205
	v_lshl_add_u32 v2, v0, 13, v1
	v_ashrrev_i32_e32 v3, 31, v2
	v_lshl_add_u64 v[2:3], v[2:3], 2, s[14:15]
	global_load_dword v208, v[2:3], off

.LBB0_1210:
	s_and_b64 vcc, exec, s[4:5]
	s_cbranch_vccnz .LBB0_1220
	v_readlane_b32 s6, v255, 3
	s_mul_i32 s16, s22, 3
	s_add_i32 s16, s16, s19
	v_mov_b32_e32 v0, s6
	ds_read_b32 v0, v0
	s_waitcnt lgkmcnt(0)
	v_cmp_ge_i32_e32 vcc, s16, v0
	s_cbranch_vccnz .LBB0_1220
	s_movk_i32 s6, 0x100
	v_cmp_gt_i32_e32 vcc, s6, v206
	s_and_saveexec_b64 s[6:7], vcc
	s_cbranch_execz .LBB0_1219
	v_readlane_b32 s17, v255, 4
	v_mov_b32_e32 v208, -1
	s_nop 0
	v_readlane_b32 s100, v255, 4
	s_nop 1
	v_mov_b32_e32 v214, s100
	ds_read2_b32 v[128:129], v214 offset1:1
	v_readlane_b32 s100, v254, 45
	s_nop 1
	v_mov_b32_e32 v214, s100
	ds_read2_b32 v[130:131], v214 offset1:1
	v_readlane_b32 s100, v254, 47
	s_nop 1
	v_mov_b32_e32 v214, s100
	ds_read2_b32 v[132:133], v214 offset1:1
	v_readlane_b32 s100, v254, 48
	s_nop 1
	v_mov_b32_e32 v214, s100
	ds_read2_b32 v[134:135], v214 offset1:1
	v_readlane_b32 s100, v254, 50
	s_nop 1
	v_mov_b32_e32 v214, s100
	ds_read2_b32 v[136:137], v214 offset1:1
	v_readlane_b32 s100, v254, 51
	s_nop 1
	v_mov_b32_e32 v214, s100
	ds_read2_b32 v[138:139], v214 offset1:1
	v_readlane_b32 s100, v254, 53
	s_nop 1
	v_mov_b32_e32 v214, s100
	ds_read2_b32 v[140:141], v214 offset1:1
	v_readlane_b32 s100, v254, 54
	s_nop 1
	v_mov_b32_e32 v214, s100
	ds_read2_b32 v[142:143], v214 offset1:1
	s_waitcnt lgkmcnt(0)
	v_readlane_b32 s100, v254, 56
	s_nop 1
	v_mov_b32_e32 v214, s100
	ds_read2_b32 v[144:145], v214 offset1:1
	v_readlane_b32 s100, v254, 57
	s_nop 1
	v_mov_b32_e32 v214, s100
	ds_read2_b32 v[146:147], v214 offset1:1
	v_readlane_b32 s100, v254, 59
	s_nop 1
	v_mov_b32_e32 v214, s100
	ds_read2_b32 v[148:149], v214 offset1:1
	v_readlane_b32 s100, v254, 60
	s_nop 1
	v_mov_b32_e32 v214, s100
	ds_read2_b32 v[150:151], v214 offset1:1
	v_readlane_b32 s100, v254, 62
	s_nop 1
	v_mov_b32_e32 v214, s100
	ds_read2_b32 v[152:153], v214 offset1:1
	v_readlane_b32 s100, v254, 63
	s_nop 1
	v_mov_b32_e32 v214, s100
	ds_read2_b32 v[154:155], v214 offset1:1
	v_readlane_b32 s100, v255, 1
	s_nop 1
	v_mov_b32_e32 v214, s100
	ds_read2_b32 v[156:157], v214 offset1:1
	s_waitcnt lgkmcnt(0)
	v_mov_b32_e32 v0, v128
	v_mov_b32_e32 v1, v129
	v_readlane_b32 s17, v254, 45
	s_waitcnt lgkmcnt(0)
	v_cmp_ge_i32_e32 vcc, s16, v0
	s_nop 1
	v_cndmask_b32_e64 v0, 0, 1, vcc
	v_cmp_lt_i32_e32 vcc, s16, v1
	s_nop 1
	v_cndmask_b32_e32 v2, 2, v0, vcc
	v_mov_b32_e32 v0, v130
	v_mov_b32_e32 v1, v131
	v_readlane_b32 s17, v254, 47
	s_waitcnt lgkmcnt(0)
	v_cmp_lt_i32_e32 vcc, s16, v0
	s_nop 1
	v_cndmask_b32_e32 v0, 3, v2, vcc
	v_cmp_lt_i32_e32 vcc, s16, v1
	s_nop 1
	v_cndmask_b32_e32 v2, 4, v0, vcc
	v_mov_b32_e32 v0, v132
	v_mov_b32_e32 v1, v133
	v_readlane_b32 s17, v254, 48
	s_waitcnt lgkmcnt(0)
	v_cmp_lt_i32_e32 vcc, s16, v0
	s_nop 1
	v_cndmask_b32_e32 v0, 5, v2, vcc
	v_cmp_lt_i32_e32 vcc, s16, v1
	s_nop 1
	v_cndmask_b32_e32 v2, 6, v0, vcc
	v_mov_b32_e32 v0, v134
	v_mov_b32_e32 v1, v135
	v_readlane_b32 s17, v254, 50
	s_waitcnt lgkmcnt(0)
	v_cmp_lt_i32_e32 vcc, s16, v0
	s_nop 1
	v_cndmask_b32_e32 v0, 7, v2, vcc
	v_cmp_lt_i32_e32 vcc, s16, v1
	s_nop 1
	v_cndmask_b32_e32 v2, 8, v0, vcc
	v_mov_b32_e32 v0, v136
	v_mov_b32_e32 v1, v137
	v_readlane_b32 s17, v254, 51
	s_waitcnt lgkmcnt(0)
	v_cmp_lt_i32_e32 vcc, s16, v0
	s_nop 1
	v_cndmask_b32_e32 v0, 9, v2, vcc
	v_cmp_lt_i32_e32 vcc, s16, v1
	s_nop 1
	v_cndmask_b32_e32 v2, 10, v0, vcc
	v_mov_b32_e32 v0, v138
	v_mov_b32_e32 v1, v139
	v_readlane_b32 s17, v254, 53
	s_waitcnt lgkmcnt(0)
	v_cmp_lt_i32_e32 vcc, s16, v0
	s_nop 1
	v_cndmask_b32_e32 v0, 11, v2, vcc
	v_cmp_lt_i32_e32 vcc, s16, v1
	s_nop 1
	v_cndmask_b32_e32 v2, 12, v0, vcc
	v_mov_b32_e32 v0, v140
	v_mov_b32_e32 v1, v141
	v_readlane_b32 s17, v254, 54
	s_waitcnt lgkmcnt(0)
	v_cmp_lt_i32_e32 vcc, s16, v0
	s_nop 1
	v_cndmask_b32_e32 v0, 13, v2, vcc
	v_cmp_lt_i32_e32 vcc, s16, v1
	s_nop 1
	v_cndmask_b32_e32 v2, 14, v0, vcc
	v_mov_b32_e32 v0, v142
	v_mov_b32_e32 v1, v143
	v_readlane_b32 s17, v254, 56
	s_waitcnt lgkmcnt(0)
	v_cmp_lt_i32_e32 vcc, s16, v0
	s_nop 1
	v_cndmask_b32_e32 v0, 15, v2, vcc
	v_cmp_lt_i32_e32 vcc, s16, v1
	s_nop 1
	v_cndmask_b32_e32 v2, 16, v0, vcc
	v_mov_b32_e32 v0, v144
	v_mov_b32_e32 v1, v145
	v_readlane_b32 s17, v254, 57
	s_waitcnt lgkmcnt(0)
	v_cmp_lt_i32_e32 vcc, s16, v0
	s_nop 1
	v_cndmask_b32_e32 v0, 17, v2, vcc
	v_cmp_lt_i32_e32 vcc, s16, v1
	s_nop 1
	v_cndmask_b32_e32 v2, 18, v0, vcc
	v_mov_b32_e32 v0, v146
	v_mov_b32_e32 v1, v147
	v_readlane_b32 s17, v254, 59
	s_waitcnt lgkmcnt(0)
	v_cmp_lt_i32_e32 vcc, s16, v0
	s_nop 1
	v_cndmask_b32_e32 v0, 19, v2, vcc
	v_cmp_lt_i32_e32 vcc, s16, v1
	s_nop 1
	v_cndmask_b32_e32 v2, 20, v0, vcc
	v_mov_b32_e32 v0, v148
	v_mov_b32_e32 v1, v149
	v_readlane_b32 s17, v254, 60
	s_waitcnt lgkmcnt(0)
	v_cmp_lt_i32_e32 vcc, s16, v0
	s_nop 1
	v_cndmask_b32_e32 v0, 21, v2, vcc
	v_cmp_lt_i32_e32 vcc, s16, v1
	s_nop 1
	v_cndmask_b32_e32 v2, 22, v0, vcc
	v_mov_b32_e32 v0, v150
	v_mov_b32_e32 v1, v151
	v_readlane_b32 s17, v254, 62
	s_waitcnt lgkmcnt(0)
	v_cmp_lt_i32_e32 vcc, s16, v0
	s_nop 1
	v_cndmask_b32_e32 v0, 23, v2, vcc
	v_cmp_lt_i32_e32 vcc, s16, v1
	s_nop 1
	v_cndmask_b32_e32 v2, 24, v0, vcc
	v_mov_b32_e32 v0, v152
	v_mov_b32_e32 v1, v153
	v_readlane_b32 s17, v254, 63
	s_waitcnt lgkmcnt(0)
	v_cmp_lt_i32_e32 vcc, s16, v0
	s_nop 1
	v_cndmask_b32_e32 v0, 25, v2, vcc
	v_cmp_lt_i32_e32 vcc, s16, v1
	s_nop 1
	v_cndmask_b32_e32 v2, 26, v0, vcc
	v_mov_b32_e32 v0, v154
	v_mov_b32_e32 v1, v155
	v_readlane_b32 s17, v255, 1
	s_waitcnt lgkmcnt(0)
	v_cmp_lt_i32_e32 vcc, s16, v0
	s_nop 1
	v_cndmask_b32_e32 v0, 27, v2, vcc
	v_cmp_lt_i32_e32 vcc, s16, v1
	s_nop 1
	v_cndmask_b32_e32 v2, 28, v0, vcc
	v_mov_b32_e32 v0, v156
	v_mov_b32_e32 v1, v157
	v_readlane_b32 s17, v255, 2
	s_waitcnt lgkmcnt(0)
	v_cmp_lt_i32_e32 vcc, s16, v0
	s_nop 1
	v_cndmask_b32_e32 v0, 29, v2, vcc
	v_cmp_lt_i32_e32 vcc, s16, v1
	v_mov_b32_e32 v1, s17
	ds_read_b32 v1, v1
	v_cndmask_b32_e32 v0, 30, v0, vcc
	s_waitcnt lgkmcnt(0)
	v_cmp_lt_i32_e32 vcc, s16, v1
	s_nop 1
	v_cndmask_b32_e32 v0, 31, v0, vcc
	v_lshlrev_b32_e32 v1, 2, v0
	v_add_u32_e32 v1, 0, v1
	v_add_u32_e32 v2, 0x24000, v1
	ds_read_b32 v2, v2
	v_add_u32_e32 v1, 0x24100, v1
	ds_read_b32 v1, v1
	s_waitcnt lgkmcnt(1)
	v_readfirstlane_b32 s17, v2
	s_addk_i32 s17, 0xff
	s_ashr_i32 s17, s17, 8
	s_abs_i32 s25, s17
	s_waitcnt lgkmcnt(0)
	v_readfirstlane_b32 s23, v1
	v_cvt_f32_u32_e32 v1, s25
	s_sub_i32 s26, 0, s25
	s_sub_i32 s16, s16, s23
	s_abs_i32 s24, s16
	v_rcp_iflag_f32_e32 v1, v1
	s_xor_b32 s23, s16, s17
	s_ashr_i32 s23, s23, 31
	v_mul_f32_e32 v1, 0x4f7ffffe, v1
	v_cvt_u32_f32_e32 v1, v1
	s_nop 0
	v_readfirstlane_b32 s27, v1
	s_mul_i32 s26, s26, s27
	s_mul_hi_u32 s26, s27, s26
	s_add_i32 s27, s27, s26
	s_mul_hi_u32 s26, s24, s27
	s_mul_i32 s27, s26, s25
	s_sub_i32 s24, s24, s27
	s_add_i32 s27, s26, 1
	s_sub_i32 s28, s24, s25
	s_cmp_ge_u32 s24, s25
	s_cselect_b32 s26, s27, s26
	s_cselect_b32 s24, s28, s24
	s_add_i32 s27, s26, 1
	s_cmp_ge_u32 s24, s25
	s_cselect_b32 s24, s27, s26
	s_xor_b32 s24, s24, s23
	s_sub_i32 s23, s24, s23
	s_mul_i32 s17, s23, s17
	s_sub_i32 s24, s16, s17
	v_lshl_add_u32 v1, s24, 8, v206
	v_cmp_lt_i32_e32 vcc, v1, v2
	s_and_saveexec_b64 s[16:17], vcc
	s_cbranch_execz .LBB0_1215
	v_lshl_add_u32 v2, v0, 13, v1
	v_ashrrev_i32_e32 v3, 31, v2
	v_lshl_add_u64 v[2:3], v[2:3], 2, s[14:15]
	global_load_dword v208, v[2:3], off

.LBB0_1220:
	s_and_b64 vcc, exec, s[4:5]
	s_cbranch_vccnz .LBB0_1230
	v_readlane_b32 s6, v255, 3
	s_lshl_b32 s16, s22, 2
	s_add_i32 s16, s16, s19
	v_mov_b32_e32 v0, s6
	ds_read_b32 v0, v0
	s_waitcnt lgkmcnt(0)
	v_cmp_ge_i32_e32 vcc, s16, v0
	s_cbranch_vccnz .LBB0_1230
	s_movk_i32 s6, 0x100
	v_cmp_gt_i32_e32 vcc, s6, v206
	s_and_saveexec_b64 s[6:7], vcc
	s_cbranch_execz .LBB0_1229
	v_readlane_b32 s17, v255, 4
	v_mov_b32_e32 v208, -1
	s_nop 0
	v_readlane_b32 s100, v255, 4
	s_nop 1
	v_mov_b32_e32 v214, s100
	ds_read2_b32 v[128:129], v214 offset1:1
	v_readlane_b32 s100, v254, 45
	s_nop 1
	v_mov_b32_e32 v214, s100
	ds_read2_b32 v[130:131], v214 offset1:1
	v_readlane_b32 s100, v254, 47
	s_nop 1
	v_mov_b32_e32 v214, s100
	ds_read2_b32 v[132:133], v214 offset1:1
	v_readlane_b32 s100, v254, 48
	s_nop 1
	v_mov_b32_e32 v214, s100
	ds_read2_b32 v[134:135], v214 offset1:1
	v_readlane_b32 s100, v254, 50
	s_nop 1
	v_mov_b32_e32 v214, s100
	ds_read2_b32 v[136:137], v214 offset1:1
	v_readlane_b32 s100, v254, 51
	s_nop 1
	v_mov_b32_e32 v214, s100
	ds_read2_b32 v[138:139], v214 offset1:1
	v_readlane_b32 s100, v254, 53
	s_nop 1
	v_mov_b32_e32 v214, s100
	ds_read2_b32 v[140:141], v214 offset1:1
	v_readlane_b32 s100, v254, 54
	s_nop 1
	v_mov_b32_e32 v214, s100
	ds_read2_b32 v[142:143], v214 offset1:1
	s_waitcnt lgkmcnt(0)
	v_readlane_b32 s100, v254, 56
	s_nop 1
	v_mov_b32_e32 v214, s100
	ds_read2_b32 v[144:145], v214 offset1:1
	v_readlane_b32 s100, v254, 57
	s_nop 1
	v_mov_b32_e32 v214, s100
	ds_read2_b32 v[146:147], v214 offset1:1
	v_readlane_b32 s100, v254, 59
	s_nop 1
	v_mov_b32_e32 v214, s100
	ds_read2_b32 v[148:149], v214 offset1:1
	v_readlane_b32 s100, v254, 60
	s_nop 1
	v_mov_b32_e32 v214, s100
	ds_read2_b32 v[150:151], v214 offset1:1
	v_readlane_b32 s100, v254, 62
	s_nop 1
	v_mov_b32_e32 v214, s100
	ds_read2_b32 v[152:153], v214 offset1:1
	v_readlane_b32 s100, v254, 63
	s_nop 1
	v_mov_b32_e32 v214, s100
	ds_read2_b32 v[154:155], v214 offset1:1
	v_readlane_b32 s100, v255, 1
	s_nop 1
	v_mov_b32_e32 v214, s100
	ds_read2_b32 v[156:157], v214 offset1:1
	s_waitcnt lgkmcnt(0)
	v_mov_b32_e32 v0, v128
	v_mov_b32_e32 v1, v129
	v_readlane_b32 s17, v254, 45
	s_waitcnt lgkmcnt(0)
	v_cmp_ge_i32_e32 vcc, s16, v0
	s_nop 1
	v_cndmask_b32_e64 v0, 0, 1, vcc
	v_cmp_lt_i32_e32 vcc, s16, v1
	s_nop 1
	v_cndmask_b32_e32 v2, 2, v0, vcc
	v_mov_b32_e32 v0, v130
	v_mov_b32_e32 v1, v131
	v_readlane_b32 s17, v254, 47
	s_waitcnt lgkmcnt(0)
	v_cmp_lt_i32_e32 vcc, s16, v0
	s_nop 1
	v_cndmask_b32_e32 v0, 3, v2, vcc
	v_cmp_lt_i32_e32 vcc, s16, v1
	s_nop 1
	v_cndmask_b32_e32 v2, 4, v0, vcc
	v_mov_b32_e32 v0, v132
	v_mov_b32_e32 v1, v133
	v_readlane_b32 s17, v254, 48
	s_waitcnt lgkmcnt(0)
	v_cmp_lt_i32_e32 vcc, s16, v0
	s_nop 1
	v_cndmask_b32_e32 v0, 5, v2, vcc
	v_cmp_lt_i32_e32 vcc, s16, v1
	s_nop 1
	v_cndmask_b32_e32 v2, 6, v0, vcc
	v_mov_b32_e32 v0, v134
	v_mov_b32_e32 v1, v135
	v_readlane_b32 s17, v254, 50
	s_waitcnt lgkmcnt(0)
	v_cmp_lt_i32_e32 vcc, s16, v0
	s_nop 1
	v_cndmask_b32_e32 v0, 7, v2, vcc
	v_cmp_lt_i32_e32 vcc, s16, v1
	s_nop 1
	v_cndmask_b32_e32 v2, 8, v0, vcc
	v_mov_b32_e32 v0, v136
	v_mov_b32_e32 v1, v137
	v_readlane_b32 s17, v254, 51
	s_waitcnt lgkmcnt(0)
	v_cmp_lt_i32_e32 vcc, s16, v0
	s_nop 1
	v_cndmask_b32_e32 v0, 9, v2, vcc
	v_cmp_lt_i32_e32 vcc, s16, v1
	s_nop 1
	v_cndmask_b32_e32 v2, 10, v0, vcc
	v_mov_b32_e32 v0, v138
	v_mov_b32_e32 v1, v139
	v_readlane_b32 s17, v254, 53
	s_waitcnt lgkmcnt(0)
	v_cmp_lt_i32_e32 vcc, s16, v0
	s_nop 1
	v_cndmask_b32_e32 v0, 11, v2, vcc
	v_cmp_lt_i32_e32 vcc, s16, v1
	s_nop 1
	v_cndmask_b32_e32 v2, 12, v0, vcc
	v_mov_b32_e32 v0, v140
	v_mov_b32_e32 v1, v141
	v_readlane_b32 s17, v254, 54
	s_waitcnt lgkmcnt(0)
	v_cmp_lt_i32_e32 vcc, s16, v0
	s_nop 1
	v_cndmask_b32_e32 v0, 13, v2, vcc
	v_cmp_lt_i32_e32 vcc, s16, v1
	s_nop 1
	v_cndmask_b32_e32 v2, 14, v0, vcc
	v_mov_b32_e32 v0, v142
	v_mov_b32_e32 v1, v143
	v_readlane_b32 s17, v254, 56
	s_waitcnt lgkmcnt(0)
	v_cmp_lt_i32_e32 vcc, s16, v0
	s_nop 1
	v_cndmask_b32_e32 v0, 15, v2, vcc
	v_cmp_lt_i32_e32 vcc, s16, v1
	s_nop 1
	v_cndmask_b32_e32 v2, 16, v0, vcc
	v_mov_b32_e32 v0, v144
	v_mov_b32_e32 v1, v145
	v_readlane_b32 s17, v254, 57
	s_waitcnt lgkmcnt(0)
	v_cmp_lt_i32_e32 vcc, s16, v0
	s_nop 1
	v_cndmask_b32_e32 v0, 17, v2, vcc
	v_cmp_lt_i32_e32 vcc, s16, v1
	s_nop 1
	v_cndmask_b32_e32 v2, 18, v0, vcc
	v_mov_b32_e32 v0, v146
	v_mov_b32_e32 v1, v147
	v_readlane_b32 s17, v254, 59
	s_waitcnt lgkmcnt(0)
	v_cmp_lt_i32_e32 vcc, s16, v0
	s_nop 1
	v_cndmask_b32_e32 v0, 19, v2, vcc
	v_cmp_lt_i32_e32 vcc, s16, v1
	s_nop 1
	v_cndmask_b32_e32 v2, 20, v0, vcc
	v_mov_b32_e32 v0, v148
	v_mov_b32_e32 v1, v149
	v_readlane_b32 s17, v254, 60
	s_waitcnt lgkmcnt(0)
	v_cmp_lt_i32_e32 vcc, s16, v0
	s_nop 1
	v_cndmask_b32_e32 v0, 21, v2, vcc
	v_cmp_lt_i32_e32 vcc, s16, v1
	s_nop 1
	v_cndmask_b32_e32 v2, 22, v0, vcc
	v_mov_b32_e32 v0, v150
	v_mov_b32_e32 v1, v151
	v_readlane_b32 s17, v254, 62
	s_waitcnt lgkmcnt(0)
	v_cmp_lt_i32_e32 vcc, s16, v0
	s_nop 1
	v_cndmask_b32_e32 v0, 23, v2, vcc
	v_cmp_lt_i32_e32 vcc, s16, v1
	s_nop 1
	v_cndmask_b32_e32 v2, 24, v0, vcc
	v_mov_b32_e32 v0, v152
	v_mov_b32_e32 v1, v153
	v_readlane_b32 s17, v254, 63
	s_waitcnt lgkmcnt(0)
	v_cmp_lt_i32_e32 vcc, s16, v0
	s_nop 1
	v_cndmask_b32_e32 v0, 25, v2, vcc
	v_cmp_lt_i32_e32 vcc, s16, v1
	s_nop 1
	v_cndmask_b32_e32 v2, 26, v0, vcc
	v_mov_b32_e32 v0, v154
	v_mov_b32_e32 v1, v155
	v_readlane_b32 s17, v255, 1
	s_waitcnt lgkmcnt(0)
	v_cmp_lt_i32_e32 vcc, s16, v0
	s_nop 1
	v_cndmask_b32_e32 v0, 27, v2, vcc
	v_cmp_lt_i32_e32 vcc, s16, v1
	s_nop 1
	v_cndmask_b32_e32 v2, 28, v0, vcc
	v_mov_b32_e32 v0, v156
	v_mov_b32_e32 v1, v157
	v_readlane_b32 s17, v255, 2
	s_waitcnt lgkmcnt(0)
	v_cmp_lt_i32_e32 vcc, s16, v0
	s_nop 1
	v_cndmask_b32_e32 v0, 29, v2, vcc
	v_cmp_lt_i32_e32 vcc, s16, v1
	v_mov_b32_e32 v1, s17
	ds_read_b32 v1, v1
	v_cndmask_b32_e32 v0, 30, v0, vcc
	s_waitcnt lgkmcnt(0)
	v_cmp_lt_i32_e32 vcc, s16, v1
	s_nop 1
	v_cndmask_b32_e32 v0, 31, v0, vcc
	v_lshlrev_b32_e32 v1, 2, v0
	v_add_u32_e32 v1, 0, v1
	v_add_u32_e32 v2, 0x24000, v1
	ds_read_b32 v2, v2
	v_add_u32_e32 v1, 0x24100, v1
	ds_read_b32 v1, v1
	s_waitcnt lgkmcnt(1)
	v_readfirstlane_b32 s17, v2
	s_addk_i32 s17, 0xff
	s_ashr_i32 s17, s17, 8
	s_abs_i32 s25, s17
	s_waitcnt lgkmcnt(0)
	v_readfirstlane_b32 s23, v1
	v_cvt_f32_u32_e32 v1, s25
	s_sub_i32 s26, 0, s25
	s_sub_i32 s16, s16, s23
	s_abs_i32 s24, s16
	v_rcp_iflag_f32_e32 v1, v1
	s_xor_b32 s23, s16, s17
	s_ashr_i32 s23, s23, 31
	v_mul_f32_e32 v1, 0x4f7ffffe, v1
	v_cvt_u32_f32_e32 v1, v1
	s_nop 0
	v_readfirstlane_b32 s27, v1
	s_mul_i32 s26, s26, s27
	s_mul_hi_u32 s26, s27, s26
	s_add_i32 s27, s27, s26
	s_mul_hi_u32 s26, s24, s27
	s_mul_i32 s27, s26, s25
	s_sub_i32 s24, s24, s27
	s_add_i32 s27, s26, 1
	s_sub_i32 s28, s24, s25
	s_cmp_ge_u32 s24, s25
	s_cselect_b32 s26, s27, s26
	s_cselect_b32 s24, s28, s24
	s_add_i32 s27, s26, 1
	s_cmp_ge_u32 s24, s25
	s_cselect_b32 s24, s27, s26
	s_xor_b32 s24, s24, s23
	s_sub_i32 s23, s24, s23
	s_mul_i32 s17, s23, s17
	s_sub_i32 s24, s16, s17
	v_lshl_add_u32 v1, s24, 8, v206
	v_cmp_lt_i32_e32 vcc, v1, v2
	s_and_saveexec_b64 s[16:17], vcc
	s_cbranch_execz .LBB0_1225
	v_lshl_add_u32 v2, v0, 13, v1
	v_ashrrev_i32_e32 v3, 31, v2
	v_lshl_add_u64 v[2:3], v[2:3], 2, s[14:15]
	global_load_dword v208, v[2:3], off

.LBB0_1230:
	s_and_b64 vcc, exec, s[4:5]
	s_cbranch_vccnz .LBB0_1242
	v_readlane_b32 s4, v255, 3
	s_mul_i32 s6, s22, 5
	s_add_i32 s6, s6, s19
	v_mov_b32_e32 v0, s4
	ds_read_b32 v0, v0
	s_waitcnt lgkmcnt(0)
	v_cmp_lt_i32_e32 vcc, s6, v0
	v_cmp_ge_i32_e64 s[4:5], s6, v0
	s_cbranch_vccz .LBB0_1241
	v_readlane_b32 s7, v255, 4
	s_nop 1
	v_readlane_b32 s100, v255, 4
	s_nop 1
	v_mov_b32_e32 v214, s100
	ds_read2_b32 v[128:129], v214 offset1:1
	v_readlane_b32 s100, v254, 45
	s_nop 1
	v_mov_b32_e32 v214, s100
	ds_read2_b32 v[130:131], v214 offset1:1
	v_readlane_b32 s100, v254, 47
	s_nop 1
	v_mov_b32_e32 v214, s100
	ds_read2_b32 v[132:133], v214 offset1:1
	v_readlane_b32 s100, v254, 48
	s_nop 1
	v_mov_b32_e32 v214, s100
	ds_read2_b32 v[134:135], v214 offset1:1
	v_readlane_b32 s100, v254, 50
	s_nop 1
	v_mov_b32_e32 v214, s100
	ds_read2_b32 v[136:137], v214 offset1:1
	v_readlane_b32 s100, v254, 51
	s_nop 1
	v_mov_b32_e32 v214, s100
	ds_read2_b32 v[138:139], v214 offset1:1
	v_readlane_b32 s100, v254, 53
	s_nop 1
	v_mov_b32_e32 v214, s100
	ds_read2_b32 v[140:141], v214 offset1:1
	v_readlane_b32 s100, v254, 54
	s_nop 1
	v_mov_b32_e32 v214, s100
	ds_read2_b32 v[142:143], v214 offset1:1
	s_waitcnt lgkmcnt(0)
	v_readlane_b32 s100, v254, 56
	s_nop 1
	v_mov_b32_e32 v214, s100
	ds_read2_b32 v[144:145], v214 offset1:1
	v_readlane_b32 s100, v254, 57
	s_nop 1
	v_mov_b32_e32 v214, s100
	ds_read2_b32 v[146:147], v214 offset1:1
	v_readlane_b32 s100, v254, 59
	s_nop 1
	v_mov_b32_e32 v214, s100
	ds_read2_b32 v[148:149], v214 offset1:1
	v_readlane_b32 s100, v254, 60
	s_nop 1
	v_mov_b32_e32 v214, s100
	ds_read2_b32 v[150:151], v214 offset1:1
	v_readlane_b32 s100, v254, 62
	s_nop 1
	v_mov_b32_e32 v214, s100
	ds_read2_b32 v[152:153], v214 offset1:1
	v_readlane_b32 s100, v254, 63
	s_nop 1
	v_mov_b32_e32 v214, s100
	ds_read2_b32 v[154:155], v214 offset1:1
	v_readlane_b32 s100, v255, 1
	s_nop 1
	v_mov_b32_e32 v214, s100
	ds_read2_b32 v[156:157], v214 offset1:1
	s_waitcnt lgkmcnt(0)
	v_mov_b32_e32 v0, v128
	v_mov_b32_e32 v1, v129
	v_readlane_b32 s7, v254, 45
	s_waitcnt lgkmcnt(0)
	v_cmp_ge_i32_e32 vcc, s6, v0
	s_nop 1
	v_cndmask_b32_e64 v0, 0, 1, vcc
	v_cmp_lt_i32_e32 vcc, s6, v1
	s_nop 1
	v_cndmask_b32_e32 v2, 2, v0, vcc
	v_mov_b32_e32 v0, v130
	v_mov_b32_e32 v1, v131
	v_readlane_b32 s7, v254, 47
	s_waitcnt lgkmcnt(0)
	v_cmp_lt_i32_e32 vcc, s6, v0
	s_nop 1
	v_cndmask_b32_e32 v0, 3, v2, vcc
	v_cmp_lt_i32_e32 vcc, s6, v1
	s_nop 1
	v_cndmask_b32_e32 v2, 4, v0, vcc
	v_mov_b32_e32 v0, v132
	v_mov_b32_e32 v1, v133
	v_readlane_b32 s7, v254, 48
	s_waitcnt lgkmcnt(0)
	v_cmp_lt_i32_e32 vcc, s6, v0
	s_nop 1
	v_cndmask_b32_e32 v0, 5, v2, vcc
	v_cmp_lt_i32_e32 vcc, s6, v1
	s_nop 1
	v_cndmask_b32_e32 v2, 6, v0, vcc
	v_mov_b32_e32 v0, v134
	v_mov_b32_e32 v1, v135
	v_readlane_b32 s7, v254, 50
	s_waitcnt lgkmcnt(0)
	v_cmp_lt_i32_e32 vcc, s6, v0
	s_nop 1
	v_cndmask_b32_e32 v0, 7, v2, vcc
	v_cmp_lt_i32_e32 vcc, s6, v1
	s_nop 1
	v_cndmask_b32_e32 v2, 8, v0, vcc
	v_mov_b32_e32 v0, v136
	v_mov_b32_e32 v1, v137
	v_readlane_b32 s7, v254, 51
	s_waitcnt lgkmcnt(0)
	v_cmp_lt_i32_e32 vcc, s6, v0
	s_nop 1
	v_cndmask_b32_e32 v0, 9, v2, vcc
	v_cmp_lt_i32_e32 vcc, s6, v1
	s_nop 1
	v_cndmask_b32_e32 v2, 10, v0, vcc
	v_mov_b32_e32 v0, v138
	v_mov_b32_e32 v1, v139
	v_readlane_b32 s7, v254, 53
	s_waitcnt lgkmcnt(0)
	v_cmp_lt_i32_e32 vcc, s6, v0
	s_nop 1
	v_cndmask_b32_e32 v0, 11, v2, vcc
	v_cmp_lt_i32_e32 vcc, s6, v1
	s_nop 1
	v_cndmask_b32_e32 v2, 12, v0, vcc
	v_mov_b32_e32 v0, v140
	v_mov_b32_e32 v1, v141
	v_readlane_b32 s7, v254, 54
	s_waitcnt lgkmcnt(0)
	v_cmp_lt_i32_e32 vcc, s6, v0
	s_nop 1
	v_cndmask_b32_e32 v0, 13, v2, vcc
	v_cmp_lt_i32_e32 vcc, s6, v1
	s_nop 1
	v_cndmask_b32_e32 v2, 14, v0, vcc
	v_mov_b32_e32 v0, v142
	v_mov_b32_e32 v1, v143
	v_readlane_b32 s7, v254, 56
	s_waitcnt lgkmcnt(0)
	v_cmp_lt_i32_e32 vcc, s6, v0
	s_nop 1
	v_cndmask_b32_e32 v0, 15, v2, vcc
	v_cmp_lt_i32_e32 vcc, s6, v1
	s_nop 1
	v_cndmask_b32_e32 v2, 16, v0, vcc
	v_mov_b32_e32 v0, v144
	v_mov_b32_e32 v1, v145
	v_readlane_b32 s7, v254, 57
	s_waitcnt lgkmcnt(0)
	v_cmp_lt_i32_e32 vcc, s6, v0
	s_nop 1
	v_cndmask_b32_e32 v0, 17, v2, vcc
	v_cmp_lt_i32_e32 vcc, s6, v1
	s_nop 1
	v_cndmask_b32_e32 v2, 18, v0, vcc
	v_mov_b32_e32 v0, v146
	v_mov_b32_e32 v1, v147
	v_readlane_b32 s7, v254, 59
	s_waitcnt lgkmcnt(0)
	v_cmp_lt_i32_e32 vcc, s6, v0
	s_nop 1
	v_cndmask_b32_e32 v0, 19, v2, vcc
	v_cmp_lt_i32_e32 vcc, s6, v1
	s_nop 1
	v_cndmask_b32_e32 v2, 20, v0, vcc
	v_mov_b32_e32 v0, v148
	v_mov_b32_e32 v1, v149
	v_readlane_b32 s7, v254, 60
	s_waitcnt lgkmcnt(0)
	v_cmp_lt_i32_e32 vcc, s6, v0
	s_nop 1
	v_cndmask_b32_e32 v0, 21, v2, vcc
	v_cmp_lt_i32_e32 vcc, s6, v1
	s_nop 1
	v_cndmask_b32_e32 v2, 22, v0, vcc
	v_mov_b32_e32 v0, v150
	v_mov_b32_e32 v1, v151
	v_readlane_b32 s7, v254, 62
	s_waitcnt lgkmcnt(0)
	v_cmp_lt_i32_e32 vcc, s6, v0
	s_nop 1
	v_cndmask_b32_e32 v0, 23, v2, vcc
	v_cmp_lt_i32_e32 vcc, s6, v1
	s_nop 1
	v_cndmask_b32_e32 v2, 24, v0, vcc
	v_mov_b32_e32 v0, v152
	v_mov_b32_e32 v1, v153
	v_readlane_b32 s7, v254, 63
	s_waitcnt lgkmcnt(0)
	v_cmp_lt_i32_e32 vcc, s6, v0
	s_nop 1
	v_cndmask_b32_e32 v0, 25, v2, vcc
	v_cmp_lt_i32_e32 vcc, s6, v1
	s_nop 1
	v_cndmask_b32_e32 v2, 26, v0, vcc
	v_mov_b32_e32 v0, v154
	v_mov_b32_e32 v1, v155
	v_readlane_b32 s7, v255, 1
	s_waitcnt lgkmcnt(0)
	v_cmp_lt_i32_e32 vcc, s6, v0
	s_nop 1
	v_cndmask_b32_e32 v0, 27, v2, vcc
	v_cmp_lt_i32_e32 vcc, s6, v1
	s_nop 1
	v_cndmask_b32_e32 v2, 28, v0, vcc
	v_mov_b32_e32 v0, v156
	v_mov_b32_e32 v1, v157
	v_readlane_b32 s7, v255, 2
	s_waitcnt lgkmcnt(0)
	v_cmp_lt_i32_e32 vcc, s6, v0
	s_nop 1
	v_cndmask_b32_e32 v0, 29, v2, vcc
	v_cmp_lt_i32_e32 vcc, s6, v1
	v_mov_b32_e32 v1, s7
	ds_read_b32 v1, v1
	v_cndmask_b32_e32 v0, 30, v0, vcc
	s_waitcnt lgkmcnt(0)
	v_cmp_lt_i32_e32 vcc, s6, v1
	s_nop 1
	v_cndmask_b32_e32 v0, 31, v0, vcc
	v_lshlrev_b32_e32 v1, 2, v0
	v_add_u32_e32 v2, 0, v1
	v_add_u32_e32 v1, 0x24000, v2
	ds_read_b32 v1, v1
	v_add_u32_e32 v2, 0x24100, v2
	ds_read_b32 v2, v2
	s_waitcnt lgkmcnt(1)
	v_readfirstlane_b32 s7, v1
	s_addk_i32 s7, 0xff
	s_ashr_i32 s7, s7, 8
	s_abs_i32 s19, s7
	s_waitcnt lgkmcnt(0)
	v_readfirstlane_b32 s16, v2
	v_cvt_f32_u32_e32 v2, s19
	s_sub_i32 s22, 0, s19
	s_sub_i32 s6, s6, s16
	s_abs_i32 s17, s6
	v_rcp_iflag_f32_e32 v2, v2
	s_xor_b32 s16, s6, s7
	s_ashr_i32 s16, s16, 31
	v_mul_f32_e32 v2, 0x4f7ffffe, v2
	v_cvt_u32_f32_e32 v2, v2
	s_nop 0
	v_readfirstlane_b32 s23, v2
	s_mul_i32 s22, s22, s23
	s_mul_hi_u32 s22, s23, s22
	s_add_i32 s23, s23, s22
	s_mul_hi_u32 s22, s17, s23
	s_mul_i32 s23, s22, s19
	s_sub_i32 s17, s17, s23
	s_add_i32 s23, s22, 1
	s_sub_i32 s24, s17, s19
	s_cmp_ge_u32 s17, s19
	s_cselect_b32 s22, s23, s22
	s_cselect_b32 s17, s24, s17
	s_add_i32 s23, s22, 1
	s_cmp_ge_u32 s17, s19
	s_cselect_b32 s17, s23, s22
	s_xor_b32 s17, s17, s16
	s_sub_i32 s19, s17, s16
	s_mul_i32 s7, s19, s7
	s_sub_i32 s22, s6, s7
	s_movk_i32 s6, 0x100
	v_cmp_gt_i32_e32 vcc, s6, v206
	s_and_saveexec_b64 s[6:7], vcc
	s_cbranch_execz .LBB0_1238
	v_lshl_add_u32 v2, s22, 8, v206
	v_cmp_lt_i32_e32 vcc, v2, v1
	v_mov_b32_e32 v208, -1
	s_and_saveexec_b64 s[16:17], vcc
	s_cbranch_execz .LBB0_1235
	v_lshl_add_u32 v2, v0, 13, v2
	v_ashrrev_i32_e32 v3, 31, v2
	v_lshl_add_u64 v[2:3], v[2:3], 2, s[14:15]
	global_load_dword v208, v[2:3], off
